# epistage2: LDS exchange of the GEMM epilogue stores software-pipelined (site k writes its piece, then completes and stores piece k-1 whose slab read stayed in flight across the epilogue math)
# baseline (speedup 1.0000x reference)
.LBB0_195:
	s_ashr_i32 s9, s74, 2
	s_lshl_b32 s44, s74, 8
	s_and_b32 s46, s44, 0x300
	s_mul_hi_i32 s45, s9, 0x4100000
	s_mul_i32 s9, s9, 0x4100000
	s_add_u32 s44, s60, s9
	s_addc_u32 s45, s61, s45
	s_cmp_lt_u32 s74, 4
	s_cselect_b64 vcc, -1, 0
	v_lshl_add_u32 v14, s73, 8, v201
	v_or_b32_e32 v4, s46, v202
	v_cndmask_b32_e32 v2, 1.0, v215, vcc
	v_lshlrev_b32_e32 v194, 1, v4
	v_ashrrev_i32_e32 v15, 31, v14
	v_pk_mul_f32 v[10:11], v[192:193], s[18:19] op_sel_hi:[1,0]
	v_pk_mul_f32 v[12:13], v[190:191], s[18:19] op_sel_hi:[1,0]
	v_pk_mul_f32 v[20:21], v[186:187], s[18:19] op_sel_hi:[1,0]
	v_lshl_add_u64 v[16:17], s[44:45], 0, v[194:195]
	v_lshlrev_b64 v[4:5], 11, v[14:15]
	v_pk_mul_f32 v[18:19], v[188:189], s[18:19] op_sel_hi:[1,0]
	v_pk_mul_f32 v[22:23], v[2:3], v[10:11] op_sel_hi:[0,1]
	v_pk_mul_f32 v[10:11], v[2:3], v[12:13] op_sel_hi:[0,1]
	v_pk_mul_f32 v[12:13], v[2:3], v[20:21] op_sel_hi:[0,1]
	v_lshl_add_u64 v[4:5], v[16:17], 0, v[4:5]
	v_pk_mul_f32 v[18:19], v[2:3], v[18:19] op_sel_hi:[0,1]
	v_cvt_pk_bf16_f32 v10, v10, v11
	v_cvt_pk_bf16_f32 v11, v22, v23
	v_cvt_pk_bf16_f32 v12, v12, v13
	v_cvt_pk_bf16_f32 v13, v18, v19
	ds_write_b128 v240, v[10:13]
	s_waitcnt lgkmcnt(0)
	s_barrier
	ds_read_b128 v[246:249], v241
	v_lshl_add_u64 v[244:245], v[4:5], 0, v[242:243]
	v_pk_mul_f32 v[20:21], v[178:179], s[18:19] op_sel_hi:[1,0]
	v_pk_mul_f32 v[18:19], v[180:181], s[18:19] op_sel_hi:[1,0]
	v_pk_mul_f32 v[10:11], v[184:185], s[18:19] op_sel_hi:[1,0]
	v_pk_mul_f32 v[12:13], v[182:183], s[18:19] op_sel_hi:[1,0]
	v_pk_mul_f32 v[22:23], v[2:3], v[10:11] op_sel_hi:[0,1]
	v_pk_mul_f32 v[10:11], v[2:3], v[12:13] op_sel_hi:[0,1]
	v_pk_mul_f32 v[12:13], v[2:3], v[20:21] op_sel_hi:[0,1]
	v_cvt_pk_bf16_f32 v10, v10, v11
	v_pk_mul_f32 v[18:19], v[2:3], v[18:19] op_sel_hi:[0,1]
	v_cvt_pk_bf16_f32 v11, v22, v23
	v_cvt_pk_bf16_f32 v12, v12, v13
	v_cvt_pk_bf16_f32 v13, v18, v19
	ds_write_b128 v240, v[10:13] offset:8192
	s_waitcnt lgkmcnt(1)
	global_store_dwordx4 v[244:245], v[246:249], off
	s_waitcnt lgkmcnt(0)
	s_barrier
	ds_read_b128 v[246:249], v241 offset:8192
	v_lshl_add_u64 v[244:245], v[4:5], 0, v[242:243]
	v_pk_mul_f32 v[22:23], v[170:171], s[18:19] op_sel_hi:[1,0]
	v_pk_mul_f32 v[20:21], v[172:173], s[18:19] op_sel_hi:[1,0]
	v_or_b32_e32 v10, 16, v14
	v_ashrrev_i32_e32 v11, 31, v10
	v_lshlrev_b64 v[10:11], 11, v[10:11]
	v_lshl_add_u64 v[18:19], v[16:17], 0, v[10:11]
	v_pk_mul_f32 v[10:11], v[176:177], s[18:19] op_sel_hi:[1,0]
	v_pk_mul_f32 v[12:13], v[174:175], s[18:19] op_sel_hi:[1,0]
	v_pk_mul_f32 v[24:25], v[2:3], v[10:11] op_sel_hi:[0,1]
	v_pk_mul_f32 v[10:11], v[2:3], v[12:13] op_sel_hi:[0,1]
	v_pk_mul_f32 v[12:13], v[2:3], v[22:23] op_sel_hi:[0,1]
	v_pk_mul_f32 v[20:21], v[2:3], v[20:21] op_sel_hi:[0,1]
	v_cvt_pk_bf16_f32 v10, v10, v11
	v_cvt_pk_bf16_f32 v11, v24, v25
	v_cvt_pk_bf16_f32 v12, v12, v13
	v_cvt_pk_bf16_f32 v13, v20, v21
	ds_write_b128 v240, v[10:13]
	s_waitcnt lgkmcnt(1)
	global_store_dwordx4 v[244:245], v[246:249], off offset:256
	s_waitcnt lgkmcnt(0)
	s_barrier
	ds_read_b128 v[246:249], v241
	v_lshl_add_u64 v[244:245], v[18:19], 0, v[242:243]
	v_pk_mul_f32 v[22:23], v[162:163], s[18:19] op_sel_hi:[1,0]
	v_pk_mul_f32 v[20:21], v[164:165], s[18:19] op_sel_hi:[1,0]
	v_pk_mul_f32 v[10:11], v[168:169], s[18:19] op_sel_hi:[1,0]
	v_pk_mul_f32 v[12:13], v[166:167], s[18:19] op_sel_hi:[1,0]
	v_pk_mul_f32 v[24:25], v[2:3], v[10:11] op_sel_hi:[0,1]
	v_pk_mul_f32 v[10:11], v[2:3], v[12:13] op_sel_hi:[0,1]
	v_pk_mul_f32 v[12:13], v[2:3], v[22:23] op_sel_hi:[0,1]
	v_cvt_pk_bf16_f32 v10, v10, v11
	v_pk_mul_f32 v[20:21], v[2:3], v[20:21] op_sel_hi:[0,1]
	v_cvt_pk_bf16_f32 v11, v24, v25
	v_cvt_pk_bf16_f32 v12, v12, v13
	v_cvt_pk_bf16_f32 v13, v20, v21
	ds_write_b128 v240, v[10:13] offset:8192
	s_waitcnt lgkmcnt(1)
	global_store_dwordx4 v[244:245], v[246:249], off
	s_waitcnt lgkmcnt(0)
	s_barrier
	ds_read_b128 v[246:249], v241 offset:8192
	v_lshl_add_u64 v[244:245], v[18:19], 0, v[242:243]
	v_pk_mul_f32 v[22:23], v[154:155], s[18:19] op_sel_hi:[1,0]
	v_pk_mul_f32 v[20:21], v[156:157], s[18:19] op_sel_hi:[1,0]
	v_or_b32_e32 v10, 32, v14
	v_ashrrev_i32_e32 v11, 31, v10
	v_lshlrev_b64 v[10:11], 11, v[10:11]
	v_lshl_add_u64 v[18:19], v[16:17], 0, v[10:11]
	v_pk_mul_f32 v[10:11], v[160:161], s[18:19] op_sel_hi:[1,0]
	v_pk_mul_f32 v[12:13], v[158:159], s[18:19] op_sel_hi:[1,0]
	v_pk_mul_f32 v[24:25], v[2:3], v[10:11] op_sel_hi:[0,1]
	v_pk_mul_f32 v[10:11], v[2:3], v[12:13] op_sel_hi:[0,1]
	v_pk_mul_f32 v[12:13], v[2:3], v[22:23] op_sel_hi:[0,1]
	v_pk_mul_f32 v[20:21], v[2:3], v[20:21] op_sel_hi:[0,1]
	v_cvt_pk_bf16_f32 v10, v10, v11
	v_cvt_pk_bf16_f32 v11, v24, v25
	v_cvt_pk_bf16_f32 v12, v12, v13
	v_cvt_pk_bf16_f32 v13, v20, v21
	ds_write_b128 v240, v[10:13]
	s_waitcnt lgkmcnt(1)
	global_store_dwordx4 v[244:245], v[246:249], off offset:256
	s_waitcnt lgkmcnt(0)
	s_barrier
	ds_read_b128 v[246:249], v241
	v_lshl_add_u64 v[244:245], v[18:19], 0, v[242:243]
	v_pk_mul_f32 v[22:23], v[146:147], s[18:19] op_sel_hi:[1,0]
	v_pk_mul_f32 v[20:21], v[148:149], s[18:19] op_sel_hi:[1,0]
	v_pk_mul_f32 v[10:11], v[152:153], s[18:19] op_sel_hi:[1,0]
	v_pk_mul_f32 v[12:13], v[150:151], s[18:19] op_sel_hi:[1,0]
	v_pk_mul_f32 v[24:25], v[2:3], v[10:11] op_sel_hi:[0,1]
	v_pk_mul_f32 v[10:11], v[2:3], v[12:13] op_sel_hi:[0,1]
	v_pk_mul_f32 v[12:13], v[2:3], v[22:23] op_sel_hi:[0,1]
	v_cvt_pk_bf16_f32 v10, v10, v11
	v_pk_mul_f32 v[20:21], v[2:3], v[20:21] op_sel_hi:[0,1]
	v_cvt_pk_bf16_f32 v11, v24, v25
	v_cvt_pk_bf16_f32 v12, v12, v13
	v_cvt_pk_bf16_f32 v13, v20, v21
	ds_write_b128 v240, v[10:13] offset:8192
	s_waitcnt lgkmcnt(1)
	global_store_dwordx4 v[244:245], v[246:249], off
	s_waitcnt lgkmcnt(0)
	s_barrier
	ds_read_b128 v[246:249], v241 offset:8192
	v_lshl_add_u64 v[244:245], v[18:19], 0, v[242:243]
	v_pk_mul_f32 v[18:19], v[138:139], s[18:19] op_sel_hi:[1,0]
	s_nop 0
	v_or_b32_e32 v10, 48, v14
	v_ashrrev_i32_e32 v11, 31, v10
	v_lshlrev_b64 v[10:11], 11, v[10:11]
	v_lshl_add_u64 v[14:15], v[16:17], 0, v[10:11]
	v_pk_mul_f32 v[10:11], v[144:145], s[18:19] op_sel_hi:[1,0]
	v_pk_mul_f32 v[12:13], v[142:143], s[18:19] op_sel_hi:[1,0]
	v_pk_mul_f32 v[16:17], v[140:141], s[18:19] op_sel_hi:[1,0]
	v_pk_mul_f32 v[20:21], v[2:3], v[10:11] op_sel_hi:[0,1]
	v_pk_mul_f32 v[10:11], v[2:3], v[12:13] op_sel_hi:[0,1]
	v_pk_mul_f32 v[12:13], v[2:3], v[18:19] op_sel_hi:[0,1]
	v_pk_mul_f32 v[16:17], v[2:3], v[16:17] op_sel_hi:[0,1]
	v_cvt_pk_bf16_f32 v10, v10, v11
	v_cvt_pk_bf16_f32 v11, v20, v21
	v_cvt_pk_bf16_f32 v12, v12, v13
	v_cvt_pk_bf16_f32 v13, v16, v17
	ds_write_b128 v240, v[10:13]
	s_waitcnt lgkmcnt(1)
	global_store_dwordx4 v[244:245], v[246:249], off offset:256
	s_waitcnt lgkmcnt(0)
	s_barrier
	ds_read_b128 v[246:249], v241
	v_lshl_add_u64 v[244:245], v[14:15], 0, v[242:243]
	v_pk_mul_f32 v[18:19], v[130:131], s[18:19] op_sel_hi:[1,0]
	v_pk_mul_f32 v[16:17], v[132:133], s[18:19] op_sel_hi:[1,0]
	v_pk_mul_f32 v[10:11], v[136:137], s[18:19] op_sel_hi:[1,0]
	v_pk_mul_f32 v[12:13], v[134:135], s[18:19] op_sel_hi:[1,0]
	v_pk_mul_f32 v[20:21], v[2:3], v[10:11] op_sel_hi:[0,1]
	v_pk_mul_f32 v[10:11], v[2:3], v[12:13] op_sel_hi:[0,1]
	v_pk_mul_f32 v[12:13], v[2:3], v[18:19] op_sel_hi:[0,1]
	v_pk_mul_f32 v[16:17], v[2:3], v[16:17] op_sel_hi:[0,1]
	v_cvt_pk_bf16_f32 v10, v10, v11
	v_cvt_pk_bf16_f32 v11, v20, v21
	v_cvt_pk_bf16_f32 v12, v12, v13
	v_cvt_pk_bf16_f32 v13, v16, v17
	ds_write_b128 v240, v[10:13] offset:8192
	s_waitcnt lgkmcnt(1)
	global_store_dwordx4 v[244:245], v[246:249], off
	s_waitcnt lgkmcnt(0)
	s_barrier
	ds_read_b128 v[246:249], v241 offset:8192
	v_lshl_add_u64 v[244:245], v[14:15], 0, v[242:243]
	v_pk_mul_f32 v[16:17], v[124:125], s[18:19] op_sel_hi:[1,0]
	v_pk_mul_f32 v[18:19], v[122:123], s[18:19] op_sel_hi:[1,0]
	v_pk_mul_f32 v[10:11], v[128:129], s[18:19] op_sel_hi:[1,0]
	v_pk_mul_f32 v[12:13], v[126:127], s[18:19] op_sel_hi:[1,0]
	v_pk_mul_f32 v[20:21], v[2:3], v[10:11] op_sel_hi:[0,1]
	v_pk_mul_f32 v[10:11], v[2:3], v[12:13] op_sel_hi:[0,1]
	v_pk_mul_f32 v[16:17], v[2:3], v[16:17] op_sel_hi:[0,1]
	v_pk_mul_f32 v[12:13], v[2:3], v[18:19] op_sel_hi:[0,1]
	v_cvt_pk_bf16_f32 v10, v10, v11
	v_cvt_pk_bf16_f32 v11, v20, v21
	v_cvt_pk_bf16_f32 v12, v12, v13
	v_cvt_pk_bf16_f32 v13, v16, v17
	v_add_co_u32_e32 v16, vcc, s69, v4
	v_pk_mul_f32 v[18:19], v[110:111], s[18:19] op_sel_hi:[1,0]
	s_nop 0
	v_addc_co_u32_e32 v17, vcc, 0, v5, vcc
	ds_write_b128 v240, v[10:13]
	s_waitcnt lgkmcnt(1)
	global_store_dwordx4 v[244:245], v[246:249], off offset:256
	s_waitcnt lgkmcnt(0)
	s_barrier
	ds_read_b128 v[246:249], v241
	v_lshl_add_u64 v[244:245], v[16:17], 0, v[242:243]
	v_pk_mul_f32 v[16:17], v[112:113], s[18:19] op_sel_hi:[1,0]
	v_lshl_add_u64 v[14:15], v[4:5], 0, s[20:21]
	v_pk_mul_f32 v[10:11], v[120:121], s[18:19] op_sel_hi:[1,0]
	v_pk_mul_f32 v[12:13], v[118:119], s[18:19] op_sel_hi:[1,0]
	v_pk_mul_f32 v[20:21], v[2:3], v[10:11] op_sel_hi:[0,1]
	v_pk_mul_f32 v[10:11], v[2:3], v[12:13] op_sel_hi:[0,1]
	v_pk_mul_f32 v[12:13], v[2:3], v[18:19] op_sel_hi:[0,1]
	v_pk_mul_f32 v[16:17], v[2:3], v[16:17] op_sel_hi:[0,1]
	v_cvt_pk_bf16_f32 v10, v10, v11
	v_cvt_pk_bf16_f32 v11, v20, v21
	v_cvt_pk_bf16_f32 v12, v12, v13
	v_cvt_pk_bf16_f32 v13, v16, v17
	ds_write_b128 v240, v[10:13] offset:8192
	s_waitcnt lgkmcnt(1)
	global_store_dwordx4 v[244:245], v[246:249], off
	s_waitcnt lgkmcnt(0)
	s_barrier
	ds_read_b128 v[246:249], v241 offset:8192
	v_lshl_add_u64 v[244:245], v[14:15], 0, v[242:243]
	v_pk_mul_f32 v[16:17], v[108:109], s[18:19] op_sel_hi:[1,0]
	v_pk_mul_f32 v[18:19], v[106:107], s[18:19] op_sel_hi:[1,0]
	v_pk_mul_f32 v[10:11], v[116:117], s[18:19] op_sel_hi:[1,0]
	v_pk_mul_f32 v[12:13], v[114:115], s[18:19] op_sel_hi:[1,0]
	v_pk_mul_f32 v[20:21], v[2:3], v[10:11] op_sel_hi:[0,1]
	v_pk_mul_f32 v[10:11], v[2:3], v[12:13] op_sel_hi:[0,1]
	v_pk_mul_f32 v[16:17], v[2:3], v[16:17] op_sel_hi:[0,1]
	v_pk_mul_f32 v[12:13], v[2:3], v[18:19] op_sel_hi:[0,1]
	v_cvt_pk_bf16_f32 v10, v10, v11
	v_cvt_pk_bf16_f32 v11, v20, v21
	v_cvt_pk_bf16_f32 v12, v12, v13
	v_cvt_pk_bf16_f32 v13, v16, v17
	v_add_co_u32_e32 v16, vcc, s70, v4
	v_pk_mul_f32 v[18:19], v[94:95], s[18:19] op_sel_hi:[1,0]
	s_nop 0
	v_addc_co_u32_e32 v17, vcc, 0, v5, vcc
	ds_write_b128 v240, v[10:13]
	s_waitcnt lgkmcnt(1)
	global_store_dwordx4 v[244:245], v[246:249], off offset:256
	s_waitcnt lgkmcnt(0)
	s_barrier
	ds_read_b128 v[246:249], v241
	v_lshl_add_u64 v[244:245], v[16:17], 0, v[242:243]
	v_pk_mul_f32 v[16:17], v[96:97], s[18:19] op_sel_hi:[1,0]
	v_lshl_add_u64 v[14:15], v[4:5], 0, s[28:29]
	v_pk_mul_f32 v[10:11], v[104:105], s[18:19] op_sel_hi:[1,0]
	v_pk_mul_f32 v[12:13], v[102:103], s[18:19] op_sel_hi:[1,0]
	v_pk_mul_f32 v[20:21], v[2:3], v[10:11] op_sel_hi:[0,1]
	v_pk_mul_f32 v[10:11], v[2:3], v[12:13] op_sel_hi:[0,1]
	v_pk_mul_f32 v[12:13], v[2:3], v[18:19] op_sel_hi:[0,1]
	v_pk_mul_f32 v[16:17], v[2:3], v[16:17] op_sel_hi:[0,1]
	v_cvt_pk_bf16_f32 v10, v10, v11
	v_cvt_pk_bf16_f32 v11, v20, v21
	v_cvt_pk_bf16_f32 v12, v12, v13
	v_cvt_pk_bf16_f32 v13, v16, v17
	ds_write_b128 v240, v[10:13] offset:8192
	s_waitcnt lgkmcnt(1)
	global_store_dwordx4 v[244:245], v[246:249], off
	s_waitcnt lgkmcnt(0)
	s_barrier
	ds_read_b128 v[246:249], v241 offset:8192
	v_lshl_add_u64 v[244:245], v[14:15], 0, v[242:243]
	v_pk_mul_f32 v[16:17], v[92:93], s[18:19] op_sel_hi:[1,0]
	v_pk_mul_f32 v[18:19], v[90:91], s[18:19] op_sel_hi:[1,0]
	v_pk_mul_f32 v[10:11], v[100:101], s[18:19] op_sel_hi:[1,0]
	v_pk_mul_f32 v[12:13], v[98:99], s[18:19] op_sel_hi:[1,0]
	v_pk_mul_f32 v[20:21], v[2:3], v[10:11] op_sel_hi:[0,1]
	v_pk_mul_f32 v[10:11], v[2:3], v[12:13] op_sel_hi:[0,1]
	v_pk_mul_f32 v[16:17], v[2:3], v[16:17] op_sel_hi:[0,1]
	v_pk_mul_f32 v[12:13], v[2:3], v[18:19] op_sel_hi:[0,1]
	v_cvt_pk_bf16_f32 v10, v10, v11
	v_cvt_pk_bf16_f32 v11, v20, v21
	v_cvt_pk_bf16_f32 v12, v12, v13
	v_cvt_pk_bf16_f32 v13, v16, v17
	v_add_co_u32_e32 v16, vcc, s71, v4
	v_pk_mul_f32 v[18:19], v[78:79], s[18:19] op_sel_hi:[1,0]
	s_nop 0
	v_addc_co_u32_e32 v17, vcc, 0, v5, vcc
	ds_write_b128 v240, v[10:13]
	s_waitcnt lgkmcnt(1)
	global_store_dwordx4 v[244:245], v[246:249], off offset:256
	s_waitcnt lgkmcnt(0)
	s_barrier
	ds_read_b128 v[246:249], v241
	v_lshl_add_u64 v[244:245], v[16:17], 0, v[242:243]
	v_pk_mul_f32 v[16:17], v[80:81], s[18:19] op_sel_hi:[1,0]
	v_lshl_add_u64 v[14:15], v[4:5], 0, s[38:39]
	v_pk_mul_f32 v[10:11], v[88:89], s[18:19] op_sel_hi:[1,0]
	v_pk_mul_f32 v[12:13], v[86:87], s[18:19] op_sel_hi:[1,0]
	v_pk_mul_f32 v[20:21], v[2:3], v[10:11] op_sel_hi:[0,1]
	v_pk_mul_f32 v[10:11], v[2:3], v[12:13] op_sel_hi:[0,1]
	v_pk_mul_f32 v[12:13], v[2:3], v[18:19] op_sel_hi:[0,1]
	v_pk_mul_f32 v[16:17], v[2:3], v[16:17] op_sel_hi:[0,1]
	v_cvt_pk_bf16_f32 v10, v10, v11
	v_cvt_pk_bf16_f32 v11, v20, v21
	v_cvt_pk_bf16_f32 v12, v12, v13
	v_cvt_pk_bf16_f32 v13, v16, v17
	ds_write_b128 v240, v[10:13] offset:8192
	s_waitcnt lgkmcnt(1)
	global_store_dwordx4 v[244:245], v[246:249], off
	s_waitcnt lgkmcnt(0)
	s_barrier
	ds_read_b128 v[246:249], v241 offset:8192
	v_lshl_add_u64 v[244:245], v[14:15], 0, v[242:243]
	v_pk_mul_f32 v[18:19], v[74:75], s[18:19] op_sel_hi:[1,0]
	v_lshl_add_u64 v[14:15], v[4:5], 0, s[40:41]
	v_pk_mul_f32 v[10:11], v[84:85], s[18:19] op_sel_hi:[1,0]
	v_pk_mul_f32 v[12:13], v[82:83], s[18:19] op_sel_hi:[1,0]
	v_pk_mul_f32 v[16:17], v[76:77], s[18:19] op_sel_hi:[1,0]
	v_pk_mul_f32 v[20:21], v[2:3], v[10:11] op_sel_hi:[0,1]
	v_pk_mul_f32 v[10:11], v[2:3], v[12:13] op_sel_hi:[0,1]
	v_pk_mul_f32 v[12:13], v[2:3], v[18:19] op_sel_hi:[0,1]
	v_add_co_u32_e32 v4, vcc, s72, v4
	v_pk_mul_f32 v[16:17], v[2:3], v[16:17] op_sel_hi:[0,1]
	v_cvt_pk_bf16_f32 v10, v10, v11
	v_cvt_pk_bf16_f32 v11, v20, v21
	v_cvt_pk_bf16_f32 v12, v12, v13
	v_cvt_pk_bf16_f32 v13, v16, v17
	s_nop 0
	v_addc_co_u32_e32 v5, vcc, 0, v5, vcc
	ds_write_b128 v240, v[10:13]
	s_waitcnt lgkmcnt(1)
	global_store_dwordx4 v[244:245], v[246:249], off offset:256
	s_waitcnt lgkmcnt(0)
	s_barrier
	ds_read_b128 v[246:249], v241
	v_lshl_add_u64 v[244:245], v[4:5], 0, v[242:243]
	v_pk_mul_f32 v[16:17], v[66:67], s[18:19] op_sel_hi:[1,0]
	v_pk_mul_f32 v[4:5], v[72:73], s[18:19] op_sel_hi:[1,0]
	v_pk_mul_f32 v[10:11], v[70:71], s[18:19] op_sel_hi:[1,0]
	v_pk_mul_f32 v[12:13], v[68:69], s[18:19] op_sel_hi:[1,0]
	v_pk_mul_f32 v[10:11], v[2:3], v[10:11] op_sel_hi:[0,1]
	v_pk_mul_f32 v[18:19], v[2:3], v[12:13] op_sel_hi:[0,1]
	v_pk_mul_f32 v[12:13], v[2:3], v[16:17] op_sel_hi:[0,1]
	s_andn2_b64 vcc, exec, s[42:43]
	s_mov_b64 s[42:43], -1
	v_pk_mul_f32 v[4:5], v[2:3], v[4:5] op_sel_hi:[0,1]
	v_cvt_pk_bf16_f32 v10, v10, v11
	v_cvt_pk_bf16_f32 v11, v4, v5
	v_cvt_pk_bf16_f32 v12, v12, v13
	v_cvt_pk_bf16_f32 v13, v18, v19
	ds_write_b128 v240, v[10:13] offset:8192
	s_waitcnt lgkmcnt(1)
	global_store_dwordx4 v[244:245], v[246:249], off
	s_waitcnt lgkmcnt(0)
	s_barrier
	ds_read_b128 v[246:249], v241 offset:8192
	v_lshl_add_u64 v[244:245], v[14:15], 0, v[242:243]
	s_waitcnt lgkmcnt(0)
	s_barrier
	global_store_dwordx4 v[244:245], v[246:249], off offset:256
	s_cbranch_vccnz .LBB0_173
	s_andn2_b64 vcc, exec, s[14:15]
	s_cbranch_vccnz .LBB0_172
	s_barrier
	s_branch .LBB0_172

.LBB0_452:
	v_lshl_add_u32 v12, s72, 8, v199
	v_lshl_or_b32 v2, s73, 8, v200
	v_ashrrev_i32_e32 v13, 31, v12
	v_ashrrev_i32_e32 v3, 31, v2
	v_lshlrev_b64 v[8:9], 11, v[12:13]
	v_lshl_add_u64 v[8:9], s[16:17], 0, v[8:9]
	v_lshlrev_b64 v[14:15], 1, v[2:3]
	v_lshl_add_u64 v[2:3], v[8:9], 0, v[14:15]
	v_pk_fma_f32 v[8:9], v[190:191], s[20:21], 0 op_sel_hi:[1,0,0]
	v_pk_fma_f32 v[10:11], v[192:193], s[20:21], 0 op_sel_hi:[1,0,0]
	v_cvt_pk_bf16_f32 v8, v8, v9
	v_pk_fma_f32 v[16:17], v[188:189], s[20:21], 0 op_sel_hi:[1,0,0]
	v_cvt_pk_bf16_f32 v9, v10, v11
	v_pk_fma_f32 v[18:19], v[186:187], s[20:21], 0 op_sel_hi:[1,0,0]
	v_pk_fma_f32 v[20:21], v[170:171], s[20:21], 0 op_sel_hi:[1,0,0]
	v_cvt_pk_bf16_f32 v10, v18, v19
	v_cvt_pk_bf16_f32 v11, v16, v17
	ds_write_b128 v240, v[8:11]
	s_waitcnt lgkmcnt(0)
	s_barrier
	ds_read_b128 v[246:249], v241
	v_lshl_add_u64 v[244:245], v[2:3], 0, v[242:243]
	v_pk_fma_f32 v[16:17], v[176:177], s[20:21], 0 op_sel_hi:[1,0,0]
	v_pk_fma_f32 v[18:19], v[174:175], s[20:21], 0 op_sel_hi:[1,0,0]
	v_pk_fma_f32 v[8:9], v[182:183], s[20:21], 0 op_sel_hi:[1,0,0]
	v_pk_fma_f32 v[10:11], v[184:185], s[20:21], 0 op_sel_hi:[1,0,0]
	v_cvt_pk_bf16_f32 v8, v8, v9
	s_nop 0
	v_cvt_pk_bf16_f32 v9, v10, v11
	v_cvt_pk_bf16_f32 v10, v18, v19
	v_cvt_pk_bf16_f32 v11, v16, v17
	ds_write_b128 v240, v[8:11] offset:8192
	s_waitcnt lgkmcnt(1)
	global_store_dwordx4 v[244:245], v[246:249], off
	s_waitcnt lgkmcnt(0)
	s_barrier
	ds_read_b128 v[246:249], v241 offset:8192
	v_lshl_add_u64 v[244:245], v[2:3], 0, v[242:243]
	v_pk_fma_f32 v[18:19], v[172:173], s[20:21], 0 op_sel_hi:[1,0,0]
	s_nop 0
	v_or_b32_e32 v8, 16, v12
	v_ashrrev_i32_e32 v9, 31, v8
	v_lshlrev_b64 v[8:9], 11, v[8:9]
	v_lshl_add_u64 v[8:9], s[16:17], 0, v[8:9]
	v_lshl_add_u64 v[16:17], v[8:9], 0, v[14:15]
	v_pk_fma_f32 v[8:9], v[178:179], s[20:21], 0 op_sel_hi:[1,0,0]
	v_pk_fma_f32 v[10:11], v[180:181], s[20:21], 0 op_sel_hi:[1,0,0]
	v_cvt_pk_bf16_f32 v8, v8, v9
	s_nop 0
	v_cvt_pk_bf16_f32 v9, v10, v11
	v_cvt_pk_bf16_f32 v10, v20, v21
	v_cvt_pk_bf16_f32 v11, v18, v19
	ds_write_b128 v240, v[8:11]
	s_waitcnt lgkmcnt(1)
	global_store_dwordx4 v[244:245], v[246:249], off offset:256
	s_waitcnt lgkmcnt(0)
	s_barrier
	ds_read_b128 v[246:249], v241
	v_lshl_add_u64 v[244:245], v[16:17], 0, v[242:243]
	v_pk_fma_f32 v[18:19], v[160:161], s[20:21], 0 op_sel_hi:[1,0,0]
	v_pk_fma_f32 v[20:21], v[158:159], s[20:21], 0 op_sel_hi:[1,0,0]
	v_pk_fma_f32 v[8:9], v[166:167], s[20:21], 0 op_sel_hi:[1,0,0]
	v_pk_fma_f32 v[10:11], v[168:169], s[20:21], 0 op_sel_hi:[1,0,0]
	v_cvt_pk_bf16_f32 v8, v8, v9
	s_nop 0
	v_cvt_pk_bf16_f32 v9, v10, v11
	v_cvt_pk_bf16_f32 v10, v20, v21
	v_cvt_pk_bf16_f32 v11, v18, v19
	ds_write_b128 v240, v[8:11] offset:8192
	s_waitcnt lgkmcnt(1)
	global_store_dwordx4 v[244:245], v[246:249], off
	s_waitcnt lgkmcnt(0)
	s_barrier
	ds_read_b128 v[246:249], v241 offset:8192
	v_lshl_add_u64 v[244:245], v[16:17], 0, v[242:243]
	v_pk_fma_f32 v[18:19], v[156:157], s[20:21], 0 op_sel_hi:[1,0,0]
	v_pk_fma_f32 v[20:21], v[154:155], s[20:21], 0 op_sel_hi:[1,0,0]
	v_or_b32_e32 v8, 32, v12
	v_ashrrev_i32_e32 v9, 31, v8
	v_lshlrev_b64 v[8:9], 11, v[8:9]
	v_lshl_add_u64 v[8:9], s[16:17], 0, v[8:9]
	v_lshl_add_u64 v[16:17], v[8:9], 0, v[14:15]
	v_pk_fma_f32 v[8:9], v[162:163], s[20:21], 0 op_sel_hi:[1,0,0]
	v_pk_fma_f32 v[10:11], v[164:165], s[20:21], 0 op_sel_hi:[1,0,0]
	v_cvt_pk_bf16_f32 v8, v8, v9
	s_nop 0
	v_cvt_pk_bf16_f32 v9, v10, v11
	v_cvt_pk_bf16_f32 v10, v20, v21
	v_cvt_pk_bf16_f32 v11, v18, v19
	ds_write_b128 v240, v[8:11]
	s_waitcnt lgkmcnt(1)
	global_store_dwordx4 v[244:245], v[246:249], off offset:256
	s_waitcnt lgkmcnt(0)
	s_barrier
	ds_read_b128 v[246:249], v241
	v_lshl_add_u64 v[244:245], v[16:17], 0, v[242:243]
	v_pk_fma_f32 v[18:19], v[144:145], s[20:21], 0 op_sel_hi:[1,0,0]
	v_pk_fma_f32 v[20:21], v[142:143], s[20:21], 0 op_sel_hi:[1,0,0]
	v_pk_fma_f32 v[8:9], v[150:151], s[20:21], 0 op_sel_hi:[1,0,0]
	v_pk_fma_f32 v[10:11], v[152:153], s[20:21], 0 op_sel_hi:[1,0,0]
	v_cvt_pk_bf16_f32 v8, v8, v9
	s_nop 0
	v_cvt_pk_bf16_f32 v9, v10, v11
	v_cvt_pk_bf16_f32 v10, v20, v21
	v_cvt_pk_bf16_f32 v11, v18, v19
	ds_write_b128 v240, v[8:11] offset:8192
	s_waitcnt lgkmcnt(1)
	global_store_dwordx4 v[244:245], v[246:249], off
	s_waitcnt lgkmcnt(0)
	s_barrier
	ds_read_b128 v[246:249], v241 offset:8192
	v_lshl_add_u64 v[244:245], v[16:17], 0, v[242:243]
	v_pk_fma_f32 v[16:17], v[138:139], s[20:21], 0 op_sel_hi:[1,0,0]
	s_nop 0
	v_or_b32_e32 v8, 48, v12
	v_ashrrev_i32_e32 v9, 31, v8
	v_lshlrev_b64 v[8:9], 11, v[8:9]
	v_lshl_add_u64 v[8:9], s[16:17], 0, v[8:9]
	v_lshl_add_u64 v[12:13], v[8:9], 0, v[14:15]
	v_pk_fma_f32 v[10:11], v[148:149], s[20:21], 0 op_sel_hi:[1,0,0]
	v_pk_fma_f32 v[8:9], v[146:147], s[20:21], 0 op_sel_hi:[1,0,0]
	v_pk_fma_f32 v[14:15], v[140:141], s[20:21], 0 op_sel_hi:[1,0,0]
	v_cvt_pk_bf16_f32 v8, v8, v9
	v_cvt_pk_bf16_f32 v9, v10, v11
	v_cvt_pk_bf16_f32 v10, v16, v17
	v_pk_fma_f32 v[16:17], v[130:131], s[20:21], 0 op_sel_hi:[1,0,0]
	v_cvt_pk_bf16_f32 v11, v14, v15
	ds_write_b128 v240, v[8:11]
	s_waitcnt lgkmcnt(1)
	global_store_dwordx4 v[244:245], v[246:249], off offset:256
	s_waitcnt lgkmcnt(0)
	s_barrier
	ds_read_b128 v[246:249], v241
	v_lshl_add_u64 v[244:245], v[12:13], 0, v[242:243]
	v_pk_fma_f32 v[14:15], v[132:133], s[20:21], 0 op_sel_hi:[1,0,0]
	s_nop 0
	v_pk_fma_f32 v[10:11], v[136:137], s[20:21], 0 op_sel_hi:[1,0,0]
	v_pk_fma_f32 v[8:9], v[134:135], s[20:21], 0 op_sel_hi:[1,0,0]
	s_nop 0
	v_cvt_pk_bf16_f32 v8, v8, v9
	v_cvt_pk_bf16_f32 v9, v10, v11
	v_cvt_pk_bf16_f32 v10, v16, v17
	v_cvt_pk_bf16_f32 v11, v14, v15
	ds_write_b128 v240, v[8:11] offset:8192
	s_waitcnt lgkmcnt(1)
	global_store_dwordx4 v[244:245], v[246:249], off
	s_waitcnt lgkmcnt(0)
	s_barrier
	ds_read_b128 v[246:249], v241 offset:8192
	v_lshl_add_u64 v[244:245], v[12:13], 0, v[242:243]
	v_pk_fma_f32 v[14:15], v[124:125], s[20:21], 0 op_sel_hi:[1,0,0]
	v_pk_fma_f32 v[16:17], v[122:123], s[20:21], 0 op_sel_hi:[1,0,0]
	v_pk_fma_f32 v[10:11], v[128:129], s[20:21], 0 op_sel_hi:[1,0,0]
	v_pk_fma_f32 v[8:9], v[126:127], s[20:21], 0 op_sel_hi:[1,0,0]
	v_lshl_add_u64 v[12:13], v[2:3], 0, s[28:29]
	v_cvt_pk_bf16_f32 v8, v8, v9
	v_cvt_pk_bf16_f32 v9, v10, v11
	v_cvt_pk_bf16_f32 v10, v16, v17
	v_cvt_pk_bf16_f32 v11, v14, v15
	v_add_co_u32_e32 v14, vcc, s68, v2
	v_pk_fma_f32 v[16:17], v[110:111], s[20:21], 0 op_sel_hi:[1,0,0]
	s_nop 0
	v_addc_co_u32_e32 v15, vcc, 0, v3, vcc
	ds_write_b128 v240, v[8:11]
	s_waitcnt lgkmcnt(1)
	global_store_dwordx4 v[244:245], v[246:249], off offset:256
	s_waitcnt lgkmcnt(0)
	s_barrier
	ds_read_b128 v[246:249], v241
	v_lshl_add_u64 v[244:245], v[14:15], 0, v[242:243]
	v_pk_fma_f32 v[14:15], v[112:113], s[20:21], 0 op_sel_hi:[1,0,0]
	s_nop 0
	v_pk_fma_f32 v[10:11], v[120:121], s[20:21], 0 op_sel_hi:[1,0,0]
	v_pk_fma_f32 v[8:9], v[118:119], s[20:21], 0 op_sel_hi:[1,0,0]
	s_nop 0
	v_cvt_pk_bf16_f32 v8, v8, v9
	v_cvt_pk_bf16_f32 v9, v10, v11
	v_cvt_pk_bf16_f32 v10, v16, v17
	v_cvt_pk_bf16_f32 v11, v14, v15
	ds_write_b128 v240, v[8:11] offset:8192
	s_waitcnt lgkmcnt(1)
	global_store_dwordx4 v[244:245], v[246:249], off
	s_waitcnt lgkmcnt(0)
	s_barrier
	ds_read_b128 v[246:249], v241 offset:8192
	v_lshl_add_u64 v[244:245], v[12:13], 0, v[242:243]
	v_pk_fma_f32 v[14:15], v[108:109], s[20:21], 0 op_sel_hi:[1,0,0]
	v_pk_fma_f32 v[16:17], v[106:107], s[20:21], 0 op_sel_hi:[1,0,0]
	v_pk_fma_f32 v[10:11], v[116:117], s[20:21], 0 op_sel_hi:[1,0,0]
	v_pk_fma_f32 v[8:9], v[114:115], s[20:21], 0 op_sel_hi:[1,0,0]
	v_lshl_add_u64 v[12:13], v[2:3], 0, s[38:39]
	v_cvt_pk_bf16_f32 v8, v8, v9
	v_cvt_pk_bf16_f32 v9, v10, v11
	v_cvt_pk_bf16_f32 v10, v16, v17
	v_cvt_pk_bf16_f32 v11, v14, v15
	v_add_co_u32_e32 v14, vcc, s69, v2
	v_pk_fma_f32 v[16:17], v[94:95], s[20:21], 0 op_sel_hi:[1,0,0]
	s_nop 0
	v_addc_co_u32_e32 v15, vcc, 0, v3, vcc
	ds_write_b128 v240, v[8:11]
	s_waitcnt lgkmcnt(1)
	global_store_dwordx4 v[244:245], v[246:249], off offset:256
	s_waitcnt lgkmcnt(0)
	s_barrier
	ds_read_b128 v[246:249], v241
	v_lshl_add_u64 v[244:245], v[14:15], 0, v[242:243]
	v_pk_fma_f32 v[14:15], v[96:97], s[20:21], 0 op_sel_hi:[1,0,0]
	s_nop 0
	v_pk_fma_f32 v[10:11], v[104:105], s[20:21], 0 op_sel_hi:[1,0,0]
	v_pk_fma_f32 v[8:9], v[102:103], s[20:21], 0 op_sel_hi:[1,0,0]
	s_nop 0
	v_cvt_pk_bf16_f32 v8, v8, v9
	v_cvt_pk_bf16_f32 v9, v10, v11
	v_cvt_pk_bf16_f32 v10, v16, v17
	v_cvt_pk_bf16_f32 v11, v14, v15
	ds_write_b128 v240, v[8:11] offset:8192
	s_waitcnt lgkmcnt(1)
	global_store_dwordx4 v[244:245], v[246:249], off
	s_waitcnt lgkmcnt(0)
	s_barrier
	ds_read_b128 v[246:249], v241 offset:8192
	v_lshl_add_u64 v[244:245], v[12:13], 0, v[242:243]
	v_pk_fma_f32 v[14:15], v[92:93], s[20:21], 0 op_sel_hi:[1,0,0]
	v_pk_fma_f32 v[16:17], v[90:91], s[20:21], 0 op_sel_hi:[1,0,0]
	v_pk_fma_f32 v[10:11], v[100:101], s[20:21], 0 op_sel_hi:[1,0,0]
	v_pk_fma_f32 v[8:9], v[98:99], s[20:21], 0 op_sel_hi:[1,0,0]
	v_lshl_add_u64 v[12:13], v[2:3], 0, s[40:41]
	v_cvt_pk_bf16_f32 v8, v8, v9
	v_cvt_pk_bf16_f32 v9, v10, v11
	v_cvt_pk_bf16_f32 v10, v16, v17
	v_cvt_pk_bf16_f32 v11, v14, v15
	v_add_co_u32_e32 v14, vcc, s70, v2
	v_pk_fma_f32 v[16:17], v[78:79], s[20:21], 0 op_sel_hi:[1,0,0]
	s_nop 0
	v_addc_co_u32_e32 v15, vcc, 0, v3, vcc
	ds_write_b128 v240, v[8:11]
	s_waitcnt lgkmcnt(1)
	global_store_dwordx4 v[244:245], v[246:249], off offset:256
	s_waitcnt lgkmcnt(0)
	s_barrier
	ds_read_b128 v[246:249], v241
	v_lshl_add_u64 v[244:245], v[14:15], 0, v[242:243]
	v_pk_fma_f32 v[14:15], v[80:81], s[20:21], 0 op_sel_hi:[1,0,0]
	s_nop 0
	v_pk_fma_f32 v[10:11], v[88:89], s[20:21], 0 op_sel_hi:[1,0,0]
	v_pk_fma_f32 v[8:9], v[86:87], s[20:21], 0 op_sel_hi:[1,0,0]
	s_nop 0
	v_cvt_pk_bf16_f32 v8, v8, v9
	v_cvt_pk_bf16_f32 v9, v10, v11
	v_cvt_pk_bf16_f32 v10, v16, v17
	v_cvt_pk_bf16_f32 v11, v14, v15
	ds_write_b128 v240, v[8:11] offset:8192
	s_waitcnt lgkmcnt(1)
	global_store_dwordx4 v[244:245], v[246:249], off
	s_waitcnt lgkmcnt(0)
	s_barrier
	ds_read_b128 v[246:249], v241 offset:8192
	v_lshl_add_u64 v[244:245], v[12:13], 0, v[242:243]
	v_lshl_add_u64 v[12:13], v[2:3], 0, s[42:43]
	v_add_co_u32_e32 v2, vcc, s71, v2
	v_pk_fma_f32 v[10:11], v[84:85], s[20:21], 0 op_sel_hi:[1,0,0]
	v_pk_fma_f32 v[8:9], v[82:83], s[20:21], 0 op_sel_hi:[1,0,0]
	v_pk_fma_f32 v[14:15], v[76:77], s[20:21], 0 op_sel_hi:[1,0,0]
	v_pk_fma_f32 v[16:17], v[74:75], s[20:21], 0 op_sel_hi:[1,0,0]
	v_cvt_pk_bf16_f32 v8, v8, v9
	v_cvt_pk_bf16_f32 v9, v10, v11
	v_addc_co_u32_e32 v3, vcc, 0, v3, vcc
	v_cvt_pk_bf16_f32 v10, v16, v17
	v_cvt_pk_bf16_f32 v11, v14, v15
	ds_write_b128 v240, v[8:11]
	s_waitcnt lgkmcnt(1)
	global_store_dwordx4 v[244:245], v[246:249], off offset:256
	s_waitcnt lgkmcnt(0)
	s_barrier
	ds_read_b128 v[246:249], v241
	v_lshl_add_u64 v[244:245], v[2:3], 0, v[242:243]
	s_andn2_b64 vcc, exec, s[44:45]
	s_mov_b64 s[44:45], -1
	v_pk_fma_f32 v[8:9], v[70:71], s[20:21], 0 op_sel_hi:[1,0,0]
	v_pk_fma_f32 v[10:11], v[66:67], s[20:21], 0 op_sel_hi:[1,0,0]
	v_pk_fma_f32 v[2:3], v[72:73], s[20:21], 0 op_sel_hi:[1,0,0]
	v_pk_fma_f32 v[14:15], v[68:69], s[20:21], 0 op_sel_hi:[1,0,0]
	v_cvt_pk_bf16_f32 v8, v8, v9
	v_cvt_pk_bf16_f32 v9, v2, v3
	v_cvt_pk_bf16_f32 v10, v10, v11
	s_nop 0
	v_cvt_pk_bf16_f32 v11, v14, v15
	ds_write_b128 v240, v[8:11] offset:8192
	s_waitcnt lgkmcnt(1)
	global_store_dwordx4 v[244:245], v[246:249], off
	s_waitcnt lgkmcnt(0)
	s_barrier
	ds_read_b128 v[246:249], v241 offset:8192
	v_lshl_add_u64 v[244:245], v[12:13], 0, v[242:243]
	s_waitcnt lgkmcnt(0)
	s_barrier
	global_store_dwordx4 v[244:245], v[246:249], off offset:256
	s_cbranch_vccnz .LBB0_430
	s_andn2_b64 vcc, exec, s[14:15]
	s_cbranch_vccnz .LBB0_429
	s_barrier
	s_branch .LBB0_429

.LBB0_823:
	v_lshl_add_u32 v20, s87, 8, v197
	v_ashrrev_i32_e32 v21, 31, v20
	v_lshlrev_b64 v[26:27], 11, v[20:21]
	v_lshl_add_u64 v[26:27], s[38:39], 0, v[26:27]
	v_lshlrev_b64 v[30:31], 1, v[18:19]
	v_lshl_add_u64 v[18:19], v[26:27], 0, v[30:31]
	s_waitcnt vmcnt(0)
	v_pk_fma_f32 v[26:27], v[190:191], s[44:45], v[6:7] op_sel_hi:[1,0,1]
	v_pk_fma_f32 v[28:29], v[192:193], s[44:45], v[8:9] op_sel_hi:[1,0,1]
	v_cvt_pk_bf16_f32 v26, v26, v27
	v_pk_fma_f32 v[32:33], v[188:189], s[44:45], v[4:5] op_sel_hi:[1,0,1]
	v_cvt_pk_bf16_f32 v27, v28, v29
	v_pk_fma_f32 v[34:35], v[186:187], s[44:45], v[2:3] op_sel_hi:[1,0,1]
	v_pk_fma_f32 v[36:37], v[170:171], s[44:45], v[2:3] op_sel_hi:[1,0,1]
	v_cvt_pk_bf16_f32 v28, v34, v35
	v_cvt_pk_bf16_f32 v29, v32, v33
	ds_write_b128 v240, v[26:29]
	s_waitcnt lgkmcnt(0)
	s_barrier
	ds_read_b128 v[246:249], v241
	v_lshl_add_u64 v[244:245], v[18:19], 0, v[242:243]
	v_pk_fma_f32 v[32:33], v[176:177], s[44:45], v[12:13] op_sel_hi:[1,0,1]
	v_pk_fma_f32 v[34:35], v[174:175], s[44:45], v[10:11] op_sel_hi:[1,0,1]
	v_pk_fma_f32 v[26:27], v[182:183], s[44:45], v[14:15] op_sel_hi:[1,0,1]
	v_pk_fma_f32 v[28:29], v[184:185], s[44:45], v[16:17] op_sel_hi:[1,0,1]
	v_cvt_pk_bf16_f32 v26, v26, v27
	s_mov_b64 s[4:5], 0x40000
	v_cvt_pk_bf16_f32 v27, v28, v29
	v_cvt_pk_bf16_f32 v28, v34, v35
	v_cvt_pk_bf16_f32 v29, v32, v33
	ds_write_b128 v240, v[26:29] offset:8192
	s_waitcnt lgkmcnt(1)
	global_store_dwordx4 v[244:245], v[246:249], off
	s_waitcnt lgkmcnt(0)
	s_barrier
	ds_read_b128 v[246:249], v241 offset:8192
	v_lshl_add_u64 v[244:245], v[18:19], 0, v[242:243]
	v_pk_fma_f32 v[34:35], v[172:173], s[44:45], v[4:5] op_sel_hi:[1,0,1]
	s_nop 0
	v_or_b32_e32 v26, 16, v20
	v_ashrrev_i32_e32 v27, 31, v26
	v_lshlrev_b64 v[26:27], 11, v[26:27]
	v_lshl_add_u64 v[26:27], s[38:39], 0, v[26:27]
	v_lshl_add_u64 v[32:33], v[26:27], 0, v[30:31]
	v_pk_fma_f32 v[26:27], v[178:179], s[44:45], v[6:7] op_sel_hi:[1,0,1]
	v_pk_fma_f32 v[28:29], v[180:181], s[44:45], v[8:9] op_sel_hi:[1,0,1]
	v_cvt_pk_bf16_f32 v26, v26, v27
	s_nop 0
	v_cvt_pk_bf16_f32 v27, v28, v29
	v_cvt_pk_bf16_f32 v28, v36, v37
	v_cvt_pk_bf16_f32 v29, v34, v35
	ds_write_b128 v240, v[26:29]
	s_waitcnt lgkmcnt(1)
	global_store_dwordx4 v[244:245], v[246:249], off offset:256
	s_waitcnt lgkmcnt(0)
	s_barrier
	ds_read_b128 v[246:249], v241
	v_lshl_add_u64 v[244:245], v[32:33], 0, v[242:243]
	v_pk_fma_f32 v[34:35], v[160:161], s[44:45], v[12:13] op_sel_hi:[1,0,1]
	v_pk_fma_f32 v[36:37], v[158:159], s[44:45], v[10:11] op_sel_hi:[1,0,1]
	v_pk_fma_f32 v[26:27], v[166:167], s[44:45], v[14:15] op_sel_hi:[1,0,1]
	v_pk_fma_f32 v[28:29], v[168:169], s[44:45], v[16:17] op_sel_hi:[1,0,1]
	v_cvt_pk_bf16_f32 v26, v26, v27
	s_nop 0
	v_cvt_pk_bf16_f32 v27, v28, v29
	v_cvt_pk_bf16_f32 v28, v36, v37
	v_cvt_pk_bf16_f32 v29, v34, v35
	ds_write_b128 v240, v[26:29] offset:8192
	s_waitcnt lgkmcnt(1)
	global_store_dwordx4 v[244:245], v[246:249], off
	s_waitcnt lgkmcnt(0)
	s_barrier
	ds_read_b128 v[246:249], v241 offset:8192
	v_lshl_add_u64 v[244:245], v[32:33], 0, v[242:243]
	v_pk_fma_f32 v[34:35], v[156:157], s[44:45], v[4:5] op_sel_hi:[1,0,1]
	v_pk_fma_f32 v[36:37], v[154:155], s[44:45], v[2:3] op_sel_hi:[1,0,1]
	v_or_b32_e32 v26, 32, v20
	v_ashrrev_i32_e32 v27, 31, v26
	v_lshlrev_b64 v[26:27], 11, v[26:27]
	v_lshl_add_u64 v[26:27], s[38:39], 0, v[26:27]
	v_lshl_add_u64 v[32:33], v[26:27], 0, v[30:31]
	v_pk_fma_f32 v[28:29], v[164:165], s[44:45], v[8:9] op_sel_hi:[1,0,1]
	v_pk_fma_f32 v[26:27], v[162:163], s[44:45], v[6:7] op_sel_hi:[1,0,1]
	v_or_b32_e32 v20, 48, v20
	v_cvt_pk_bf16_f32 v26, v26, v27
	v_cvt_pk_bf16_f32 v27, v28, v29
	v_cvt_pk_bf16_f32 v28, v36, v37
	v_cvt_pk_bf16_f32 v29, v34, v35
	ds_write_b128 v240, v[26:29]
	s_waitcnt lgkmcnt(1)
	global_store_dwordx4 v[244:245], v[246:249], off offset:256
	s_waitcnt lgkmcnt(0)
	s_barrier
	ds_read_b128 v[246:249], v241
	v_lshl_add_u64 v[244:245], v[32:33], 0, v[242:243]
	v_ashrrev_i32_e32 v21, 31, v20
	v_pk_fma_f32 v[34:35], v[144:145], s[44:45], v[12:13] op_sel_hi:[1,0,1]
	v_pk_fma_f32 v[28:29], v[152:153], s[44:45], v[16:17] op_sel_hi:[1,0,1]
	v_pk_fma_f32 v[26:27], v[150:151], s[44:45], v[14:15] op_sel_hi:[1,0,1]
	v_pk_fma_f32 v[36:37], v[142:143], s[44:45], v[10:11] op_sel_hi:[1,0,1]
	v_cvt_pk_bf16_f32 v26, v26, v27
	v_cvt_pk_bf16_f32 v27, v28, v29
	v_lshlrev_b64 v[20:21], 11, v[20:21]
	v_cvt_pk_bf16_f32 v28, v36, v37
	v_cvt_pk_bf16_f32 v29, v34, v35
	ds_write_b128 v240, v[26:29] offset:8192
	s_waitcnt lgkmcnt(1)
	global_store_dwordx4 v[244:245], v[246:249], off
	s_waitcnt lgkmcnt(0)
	s_barrier
	ds_read_b128 v[246:249], v241 offset:8192
	v_lshl_add_u64 v[244:245], v[32:33], 0, v[242:243]
	v_lshl_add_u64 v[20:21], s[38:39], 0, v[20:21]
	v_lshl_add_u64 v[20:21], v[20:21], 0, v[30:31]
	v_pk_fma_f32 v[28:29], v[148:149], s[44:45], v[8:9] op_sel_hi:[1,0,1]
	v_pk_fma_f32 v[26:27], v[146:147], s[44:45], v[6:7] op_sel_hi:[1,0,1]
	v_pk_fma_f32 v[30:31], v[140:141], s[44:45], v[4:5] op_sel_hi:[1,0,1]
	v_pk_fma_f32 v[32:33], v[138:139], s[44:45], v[2:3] op_sel_hi:[1,0,1]
	v_cvt_pk_bf16_f32 v26, v26, v27
	v_cvt_pk_bf16_f32 v27, v28, v29
	s_nop 0
	v_cvt_pk_bf16_f32 v28, v32, v33
	v_cvt_pk_bf16_f32 v29, v30, v31
	ds_write_b128 v240, v[26:29]
	s_waitcnt lgkmcnt(1)
	global_store_dwordx4 v[244:245], v[246:249], off offset:256
	s_waitcnt lgkmcnt(0)
	s_barrier
	ds_read_b128 v[246:249], v241
	v_lshl_add_u64 v[244:245], v[20:21], 0, v[242:243]
	v_pk_fma_f32 v[30:31], v[132:133], s[44:45], v[12:13] op_sel_hi:[1,0,1]
	v_pk_fma_f32 v[32:33], v[130:131], s[44:45], v[10:11] op_sel_hi:[1,0,1]
	v_pk_fma_f32 v[28:29], v[136:137], s[44:45], v[16:17] op_sel_hi:[1,0,1]
	v_pk_fma_f32 v[26:27], v[134:135], s[44:45], v[14:15] op_sel_hi:[1,0,1]
	s_nop 0
	v_cvt_pk_bf16_f32 v26, v26, v27
	v_cvt_pk_bf16_f32 v27, v28, v29
	v_cvt_pk_bf16_f32 v28, v32, v33
	v_cvt_pk_bf16_f32 v29, v30, v31
	ds_write_b128 v240, v[26:29] offset:8192
	s_waitcnt lgkmcnt(1)
	global_store_dwordx4 v[244:245], v[246:249], off
	s_waitcnt lgkmcnt(0)
	s_barrier
	ds_read_b128 v[246:249], v241 offset:8192
	v_lshl_add_u64 v[244:245], v[20:21], 0, v[242:243]
	v_pk_fma_f32 v[30:31], v[124:125], s[44:45], v[4:5] op_sel_hi:[1,0,1]
	v_pk_fma_f32 v[32:33], v[122:123], s[44:45], v[2:3] op_sel_hi:[1,0,1]
	v_pk_fma_f32 v[28:29], v[128:129], s[44:45], v[8:9] op_sel_hi:[1,0,1]
	v_pk_fma_f32 v[26:27], v[126:127], s[44:45], v[6:7] op_sel_hi:[1,0,1]
	v_lshl_add_u64 v[20:21], v[18:19], 0, s[4:5]
	v_cvt_pk_bf16_f32 v26, v26, v27
	v_cvt_pk_bf16_f32 v27, v28, v29
	v_cvt_pk_bf16_f32 v28, v32, v33
	v_cvt_pk_bf16_f32 v29, v30, v31
	v_add_co_u32_e32 v30, vcc, s83, v18
	v_pk_fma_f32 v[32:33], v[110:111], s[44:45], v[10:11] op_sel_hi:[1,0,1]
	s_nop 0
	v_addc_co_u32_e32 v31, vcc, 0, v19, vcc
	ds_write_b128 v240, v[26:29]
	s_waitcnt lgkmcnt(1)
	global_store_dwordx4 v[244:245], v[246:249], off offset:256
	s_waitcnt lgkmcnt(0)
	s_barrier
	ds_read_b128 v[246:249], v241
	v_lshl_add_u64 v[244:245], v[30:31], 0, v[242:243]
	v_pk_fma_f32 v[30:31], v[112:113], s[44:45], v[12:13] op_sel_hi:[1,0,1]
	s_mov_b64 s[4:5], -1
	v_pk_fma_f32 v[28:29], v[120:121], s[44:45], v[16:17] op_sel_hi:[1,0,1]
	v_pk_fma_f32 v[26:27], v[118:119], s[44:45], v[14:15] op_sel_hi:[1,0,1]
	s_nop 0
	v_cvt_pk_bf16_f32 v26, v26, v27
	v_cvt_pk_bf16_f32 v27, v28, v29
	v_cvt_pk_bf16_f32 v28, v32, v33
	v_cvt_pk_bf16_f32 v29, v30, v31
	ds_write_b128 v240, v[26:29] offset:8192
	s_waitcnt lgkmcnt(1)
	global_store_dwordx4 v[244:245], v[246:249], off
	s_waitcnt lgkmcnt(0)
	s_barrier
	ds_read_b128 v[246:249], v241 offset:8192
	v_lshl_add_u64 v[244:245], v[20:21], 0, v[242:243]
	v_pk_fma_f32 v[30:31], v[108:109], s[44:45], v[4:5] op_sel_hi:[1,0,1]
	v_pk_fma_f32 v[32:33], v[106:107], s[44:45], v[2:3] op_sel_hi:[1,0,1]
	v_pk_fma_f32 v[28:29], v[116:117], s[44:45], v[8:9] op_sel_hi:[1,0,1]
	v_pk_fma_f32 v[26:27], v[114:115], s[44:45], v[6:7] op_sel_hi:[1,0,1]
	v_lshl_add_u64 v[20:21], v[18:19], 0, s[46:47]
	v_cvt_pk_bf16_f32 v26, v26, v27
	v_cvt_pk_bf16_f32 v27, v28, v29
	v_cvt_pk_bf16_f32 v28, v32, v33
	v_cvt_pk_bf16_f32 v29, v30, v31
	v_add_co_u32_e32 v30, vcc, s84, v18
	v_pk_fma_f32 v[32:33], v[94:95], s[44:45], v[10:11] op_sel_hi:[1,0,1]
	s_nop 0
	v_addc_co_u32_e32 v31, vcc, 0, v19, vcc
	ds_write_b128 v240, v[26:29]
	s_waitcnt lgkmcnt(1)
	global_store_dwordx4 v[244:245], v[246:249], off offset:256
	s_waitcnt lgkmcnt(0)
	s_barrier
	ds_read_b128 v[246:249], v241
	v_lshl_add_u64 v[244:245], v[30:31], 0, v[242:243]
	v_pk_fma_f32 v[30:31], v[96:97], s[44:45], v[12:13] op_sel_hi:[1,0,1]
	s_nop 0
	v_pk_fma_f32 v[28:29], v[104:105], s[44:45], v[16:17] op_sel_hi:[1,0,1]
	v_pk_fma_f32 v[26:27], v[102:103], s[44:45], v[14:15] op_sel_hi:[1,0,1]
	s_nop 0
	v_cvt_pk_bf16_f32 v26, v26, v27
	v_cvt_pk_bf16_f32 v27, v28, v29
	v_cvt_pk_bf16_f32 v28, v32, v33
	v_cvt_pk_bf16_f32 v29, v30, v31
	ds_write_b128 v240, v[26:29] offset:8192
	s_waitcnt lgkmcnt(1)
	global_store_dwordx4 v[244:245], v[246:249], off
	s_waitcnt lgkmcnt(0)
	s_barrier
	ds_read_b128 v[246:249], v241 offset:8192
	v_lshl_add_u64 v[244:245], v[20:21], 0, v[242:243]
	v_pk_fma_f32 v[30:31], v[92:93], s[44:45], v[4:5] op_sel_hi:[1,0,1]
	v_pk_fma_f32 v[32:33], v[90:91], s[44:45], v[2:3] op_sel_hi:[1,0,1]
	v_pk_fma_f32 v[28:29], v[100:101], s[44:45], v[8:9] op_sel_hi:[1,0,1]
	v_pk_fma_f32 v[26:27], v[98:99], s[44:45], v[6:7] op_sel_hi:[1,0,1]
	v_lshl_add_u64 v[20:21], v[18:19], 0, s[48:49]
	v_cvt_pk_bf16_f32 v26, v26, v27
	v_cvt_pk_bf16_f32 v27, v28, v29
	v_cvt_pk_bf16_f32 v28, v32, v33
	v_cvt_pk_bf16_f32 v29, v30, v31
	v_add_co_u32_e32 v30, vcc, s85, v18
	v_pk_fma_f32 v[6:7], v[82:83], s[44:45], v[6:7] op_sel_hi:[1,0,1]
	s_nop 0
	v_addc_co_u32_e32 v31, vcc, 0, v19, vcc
	ds_write_b128 v240, v[26:29]
	s_waitcnt lgkmcnt(1)
	global_store_dwordx4 v[244:245], v[246:249], off offset:256
	s_waitcnt lgkmcnt(0)
	s_barrier
	ds_read_b128 v[246:249], v241
	v_lshl_add_u64 v[244:245], v[30:31], 0, v[242:243]
	v_pk_fma_f32 v[30:31], v[80:81], s[44:45], v[12:13] op_sel_hi:[1,0,1]
	v_pk_fma_f32 v[32:33], v[78:79], s[44:45], v[10:11] op_sel_hi:[1,0,1]
	v_pk_fma_f32 v[26:27], v[86:87], s[44:45], v[14:15] op_sel_hi:[1,0,1]
	v_pk_fma_f32 v[28:29], v[88:89], s[44:45], v[16:17] op_sel_hi:[1,0,1]
	v_cvt_pk_bf16_f32 v26, v26, v27
	v_pk_fma_f32 v[8:9], v[84:85], s[44:45], v[8:9] op_sel_hi:[1,0,1]
	v_cvt_pk_bf16_f32 v27, v28, v29
	v_cvt_pk_bf16_f32 v28, v32, v33
	v_cvt_pk_bf16_f32 v29, v30, v31
	ds_write_b128 v240, v[26:29] offset:8192
	s_waitcnt lgkmcnt(1)
	global_store_dwordx4 v[244:245], v[246:249], off
	s_waitcnt lgkmcnt(0)
	s_barrier
	ds_read_b128 v[246:249], v241 offset:8192
	v_lshl_add_u64 v[244:245], v[20:21], 0, v[242:243]
	v_lshl_add_u64 v[20:21], v[18:19], 0, s[50:51]
	s_nop 0
	v_pk_fma_f32 v[26:27], v[76:77], s[44:45], v[4:5] op_sel_hi:[1,0,1]
	v_pk_fma_f32 v[4:5], v[74:75], s[44:45], v[2:3] op_sel_hi:[1,0,1]
	v_cvt_pk_bf16_f32 v2, v6, v7
	v_add_co_u32_e32 v6, vcc, s86, v18
	v_cvt_pk_bf16_f32 v3, v8, v9
	v_cvt_pk_bf16_f32 v4, v4, v5
	v_cvt_pk_bf16_f32 v5, v26, v27
	v_pk_fma_f32 v[8:9], v[66:67], s[44:45], v[10:11] op_sel_hi:[1,0,1]
	s_nop 0
	v_addc_co_u32_e32 v7, vcc, 0, v19, vcc
	ds_write_b128 v240, v[2:5]
	s_waitcnt lgkmcnt(1)
	global_store_dwordx4 v[244:245], v[246:249], off offset:256
	s_waitcnt lgkmcnt(0)
	s_barrier
	ds_read_b128 v[246:249], v241
	v_lshl_add_u64 v[244:245], v[6:7], 0, v[242:243]
	s_andn2_b64 vcc, exec, s[54:55]
	v_pk_fma_f32 v[6:7], v[68:69], s[44:45], v[12:13] op_sel_hi:[1,0,1]
	v_pk_fma_f32 v[4:5], v[72:73], s[44:45], v[16:17] op_sel_hi:[1,0,1]
	v_pk_fma_f32 v[2:3], v[70:71], s[44:45], v[14:15] op_sel_hi:[1,0,1]
	s_nop 0
	v_cvt_pk_bf16_f32 v2, v2, v3
	v_cvt_pk_bf16_f32 v3, v4, v5
	v_cvt_pk_bf16_f32 v4, v8, v9
	v_cvt_pk_bf16_f32 v5, v6, v7
	ds_write_b128 v240, v[2:5] offset:8192
	s_waitcnt lgkmcnt(1)
	global_store_dwordx4 v[244:245], v[246:249], off
	s_waitcnt lgkmcnt(0)
	s_barrier
	ds_read_b128 v[246:249], v241 offset:8192
	v_lshl_add_u64 v[244:245], v[20:21], 0, v[242:243]
	s_waitcnt lgkmcnt(0)
	s_barrier
	global_store_dwordx4 v[244:245], v[246:249], off offset:256
	s_cbranch_vccnz .LBB0_789
	s_andn2_b64 vcc, exec, s[28:29]
	s_cbranch_vccnz .LBB0_788
	s_barrier
	s_branch .LBB0_788

.LBB0_1528:
	v_lshl_add_u32 v12, s69, 8, v198
	v_lshl_or_b32 v2, s70, 8, v199
	v_ashrrev_i32_e32 v13, 31, v12
	v_ashrrev_i32_e32 v3, 31, v2
	v_lshlrev_b64 v[8:9], 11, v[12:13]
	v_lshl_add_u64 v[8:9], s[16:17], 0, v[8:9]
	v_lshlrev_b64 v[14:15], 1, v[2:3]
	v_lshl_add_u64 v[2:3], v[8:9], 0, v[14:15]
	v_pk_fma_f32 v[8:9], v[190:191], s[20:21], 0 op_sel_hi:[1,0,0]
	v_pk_fma_f32 v[10:11], v[192:193], s[20:21], 0 op_sel_hi:[1,0,0]
	v_cvt_pk_bf16_f32 v8, v8, v9
	v_pk_fma_f32 v[16:17], v[188:189], s[20:21], 0 op_sel_hi:[1,0,0]
	v_cvt_pk_bf16_f32 v9, v10, v11
	v_pk_fma_f32 v[18:19], v[186:187], s[20:21], 0 op_sel_hi:[1,0,0]
	v_pk_fma_f32 v[20:21], v[170:171], s[20:21], 0 op_sel_hi:[1,0,0]
	v_cvt_pk_bf16_f32 v10, v18, v19
	v_cvt_pk_bf16_f32 v11, v16, v17
	ds_write_b128 v240, v[8:11]
	s_waitcnt lgkmcnt(0)
	s_barrier
	ds_read_b128 v[246:249], v241
	v_lshl_add_u64 v[244:245], v[2:3], 0, v[242:243]
	v_pk_fma_f32 v[16:17], v[176:177], s[20:21], 0 op_sel_hi:[1,0,0]
	v_pk_fma_f32 v[18:19], v[174:175], s[20:21], 0 op_sel_hi:[1,0,0]
	v_pk_fma_f32 v[8:9], v[182:183], s[20:21], 0 op_sel_hi:[1,0,0]
	v_pk_fma_f32 v[10:11], v[184:185], s[20:21], 0 op_sel_hi:[1,0,0]
	v_cvt_pk_bf16_f32 v8, v8, v9
	s_nop 0
	v_cvt_pk_bf16_f32 v9, v10, v11
	v_cvt_pk_bf16_f32 v10, v18, v19
	v_cvt_pk_bf16_f32 v11, v16, v17
	ds_write_b128 v240, v[8:11] offset:8192
	s_waitcnt lgkmcnt(1)
	global_store_dwordx4 v[244:245], v[246:249], off
	s_waitcnt lgkmcnt(0)
	s_barrier
	ds_read_b128 v[246:249], v241 offset:8192
	v_lshl_add_u64 v[244:245], v[2:3], 0, v[242:243]
	v_pk_fma_f32 v[18:19], v[172:173], s[20:21], 0 op_sel_hi:[1,0,0]
	s_nop 0
	v_or_b32_e32 v8, 16, v12
	v_ashrrev_i32_e32 v9, 31, v8
	v_lshlrev_b64 v[8:9], 11, v[8:9]
	v_lshl_add_u64 v[8:9], s[16:17], 0, v[8:9]
	v_lshl_add_u64 v[16:17], v[8:9], 0, v[14:15]
	v_pk_fma_f32 v[8:9], v[178:179], s[20:21], 0 op_sel_hi:[1,0,0]
	v_pk_fma_f32 v[10:11], v[180:181], s[20:21], 0 op_sel_hi:[1,0,0]
	v_cvt_pk_bf16_f32 v8, v8, v9
	s_nop 0
	v_cvt_pk_bf16_f32 v9, v10, v11
	v_cvt_pk_bf16_f32 v10, v20, v21
	v_cvt_pk_bf16_f32 v11, v18, v19
	ds_write_b128 v240, v[8:11]
	s_waitcnt lgkmcnt(1)
	global_store_dwordx4 v[244:245], v[246:249], off offset:256
	s_waitcnt lgkmcnt(0)
	s_barrier
	ds_read_b128 v[246:249], v241
	v_lshl_add_u64 v[244:245], v[16:17], 0, v[242:243]
	v_pk_fma_f32 v[18:19], v[160:161], s[20:21], 0 op_sel_hi:[1,0,0]
	v_pk_fma_f32 v[20:21], v[158:159], s[20:21], 0 op_sel_hi:[1,0,0]
	v_pk_fma_f32 v[8:9], v[166:167], s[20:21], 0 op_sel_hi:[1,0,0]
	v_pk_fma_f32 v[10:11], v[168:169], s[20:21], 0 op_sel_hi:[1,0,0]
	v_cvt_pk_bf16_f32 v8, v8, v9
	s_nop 0
	v_cvt_pk_bf16_f32 v9, v10, v11
	v_cvt_pk_bf16_f32 v10, v20, v21
	v_cvt_pk_bf16_f32 v11, v18, v19
	ds_write_b128 v240, v[8:11] offset:8192
	s_waitcnt lgkmcnt(1)
	global_store_dwordx4 v[244:245], v[246:249], off
	s_waitcnt lgkmcnt(0)
	s_barrier
	ds_read_b128 v[246:249], v241 offset:8192
	v_lshl_add_u64 v[244:245], v[16:17], 0, v[242:243]
	v_pk_fma_f32 v[18:19], v[156:157], s[20:21], 0 op_sel_hi:[1,0,0]
	v_pk_fma_f32 v[20:21], v[154:155], s[20:21], 0 op_sel_hi:[1,0,0]
	v_or_b32_e32 v8, 32, v12
	v_ashrrev_i32_e32 v9, 31, v8
	v_lshlrev_b64 v[8:9], 11, v[8:9]
	v_lshl_add_u64 v[8:9], s[16:17], 0, v[8:9]
	v_lshl_add_u64 v[16:17], v[8:9], 0, v[14:15]
	v_pk_fma_f32 v[8:9], v[162:163], s[20:21], 0 op_sel_hi:[1,0,0]
	v_pk_fma_f32 v[10:11], v[164:165], s[20:21], 0 op_sel_hi:[1,0,0]
	v_cvt_pk_bf16_f32 v8, v8, v9
	s_nop 0
	v_cvt_pk_bf16_f32 v9, v10, v11
	v_cvt_pk_bf16_f32 v10, v20, v21
	v_cvt_pk_bf16_f32 v11, v18, v19
	ds_write_b128 v240, v[8:11]
	s_waitcnt lgkmcnt(1)
	global_store_dwordx4 v[244:245], v[246:249], off offset:256
	s_waitcnt lgkmcnt(0)
	s_barrier
	ds_read_b128 v[246:249], v241
	v_lshl_add_u64 v[244:245], v[16:17], 0, v[242:243]
	v_pk_fma_f32 v[18:19], v[144:145], s[20:21], 0 op_sel_hi:[1,0,0]
	v_pk_fma_f32 v[20:21], v[142:143], s[20:21], 0 op_sel_hi:[1,0,0]
	v_pk_fma_f32 v[8:9], v[150:151], s[20:21], 0 op_sel_hi:[1,0,0]
	v_pk_fma_f32 v[10:11], v[152:153], s[20:21], 0 op_sel_hi:[1,0,0]
	v_cvt_pk_bf16_f32 v8, v8, v9
	s_nop 0
	v_cvt_pk_bf16_f32 v9, v10, v11
	v_cvt_pk_bf16_f32 v10, v20, v21
	v_cvt_pk_bf16_f32 v11, v18, v19
	ds_write_b128 v240, v[8:11] offset:8192
	s_waitcnt lgkmcnt(1)
	global_store_dwordx4 v[244:245], v[246:249], off
	s_waitcnt lgkmcnt(0)
	s_barrier
	ds_read_b128 v[246:249], v241 offset:8192
	v_lshl_add_u64 v[244:245], v[16:17], 0, v[242:243]
	v_pk_fma_f32 v[16:17], v[138:139], s[20:21], 0 op_sel_hi:[1,0,0]
	s_nop 0
	v_or_b32_e32 v8, 48, v12
	v_ashrrev_i32_e32 v9, 31, v8
	v_lshlrev_b64 v[8:9], 11, v[8:9]
	v_lshl_add_u64 v[8:9], s[16:17], 0, v[8:9]
	v_lshl_add_u64 v[12:13], v[8:9], 0, v[14:15]
	v_pk_fma_f32 v[10:11], v[148:149], s[20:21], 0 op_sel_hi:[1,0,0]
	v_pk_fma_f32 v[8:9], v[146:147], s[20:21], 0 op_sel_hi:[1,0,0]
	v_pk_fma_f32 v[14:15], v[140:141], s[20:21], 0 op_sel_hi:[1,0,0]
	v_cvt_pk_bf16_f32 v8, v8, v9
	v_cvt_pk_bf16_f32 v9, v10, v11
	v_cvt_pk_bf16_f32 v10, v16, v17
	v_pk_fma_f32 v[16:17], v[130:131], s[20:21], 0 op_sel_hi:[1,0,0]
	v_cvt_pk_bf16_f32 v11, v14, v15
	ds_write_b128 v240, v[8:11]
	s_waitcnt lgkmcnt(1)
	global_store_dwordx4 v[244:245], v[246:249], off offset:256
	s_waitcnt lgkmcnt(0)
	s_barrier
	ds_read_b128 v[246:249], v241
	v_lshl_add_u64 v[244:245], v[12:13], 0, v[242:243]
	v_pk_fma_f32 v[14:15], v[132:133], s[20:21], 0 op_sel_hi:[1,0,0]
	s_nop 0
	v_pk_fma_f32 v[10:11], v[136:137], s[20:21], 0 op_sel_hi:[1,0,0]
	v_pk_fma_f32 v[8:9], v[134:135], s[20:21], 0 op_sel_hi:[1,0,0]
	s_nop 0
	v_cvt_pk_bf16_f32 v8, v8, v9
	v_cvt_pk_bf16_f32 v9, v10, v11
	v_cvt_pk_bf16_f32 v10, v16, v17
	v_cvt_pk_bf16_f32 v11, v14, v15
	ds_write_b128 v240, v[8:11] offset:8192
	s_waitcnt lgkmcnt(1)
	global_store_dwordx4 v[244:245], v[246:249], off
	s_waitcnt lgkmcnt(0)
	s_barrier
	ds_read_b128 v[246:249], v241 offset:8192
	v_lshl_add_u64 v[244:245], v[12:13], 0, v[242:243]
	v_pk_fma_f32 v[14:15], v[124:125], s[20:21], 0 op_sel_hi:[1,0,0]
	v_pk_fma_f32 v[16:17], v[122:123], s[20:21], 0 op_sel_hi:[1,0,0]
	v_pk_fma_f32 v[10:11], v[128:129], s[20:21], 0 op_sel_hi:[1,0,0]
	v_pk_fma_f32 v[8:9], v[126:127], s[20:21], 0 op_sel_hi:[1,0,0]
	v_lshl_add_u64 v[12:13], v[2:3], 0, s[28:29]
	v_cvt_pk_bf16_f32 v8, v8, v9
	v_cvt_pk_bf16_f32 v9, v10, v11
	v_cvt_pk_bf16_f32 v10, v16, v17
	v_cvt_pk_bf16_f32 v11, v14, v15
	v_add_co_u32_e32 v14, vcc, s65, v2
	v_pk_fma_f32 v[16:17], v[110:111], s[20:21], 0 op_sel_hi:[1,0,0]
	s_nop 0
	v_addc_co_u32_e32 v15, vcc, 0, v3, vcc
	ds_write_b128 v240, v[8:11]
	s_waitcnt lgkmcnt(1)
	global_store_dwordx4 v[244:245], v[246:249], off offset:256
	s_waitcnt lgkmcnt(0)
	s_barrier
	ds_read_b128 v[246:249], v241
	v_lshl_add_u64 v[244:245], v[14:15], 0, v[242:243]
	v_pk_fma_f32 v[14:15], v[112:113], s[20:21], 0 op_sel_hi:[1,0,0]
	s_nop 0
	v_pk_fma_f32 v[10:11], v[120:121], s[20:21], 0 op_sel_hi:[1,0,0]
	v_pk_fma_f32 v[8:9], v[118:119], s[20:21], 0 op_sel_hi:[1,0,0]
	s_nop 0
	v_cvt_pk_bf16_f32 v8, v8, v9
	v_cvt_pk_bf16_f32 v9, v10, v11
	v_cvt_pk_bf16_f32 v10, v16, v17
	v_cvt_pk_bf16_f32 v11, v14, v15
	ds_write_b128 v240, v[8:11] offset:8192
	s_waitcnt lgkmcnt(1)
	global_store_dwordx4 v[244:245], v[246:249], off
	s_waitcnt lgkmcnt(0)
	s_barrier
	ds_read_b128 v[246:249], v241 offset:8192
	v_lshl_add_u64 v[244:245], v[12:13], 0, v[242:243]
	v_pk_fma_f32 v[14:15], v[108:109], s[20:21], 0 op_sel_hi:[1,0,0]
	v_pk_fma_f32 v[16:17], v[106:107], s[20:21], 0 op_sel_hi:[1,0,0]
	v_pk_fma_f32 v[10:11], v[116:117], s[20:21], 0 op_sel_hi:[1,0,0]
	v_pk_fma_f32 v[8:9], v[114:115], s[20:21], 0 op_sel_hi:[1,0,0]
	v_lshl_add_u64 v[12:13], v[2:3], 0, s[36:37]
	v_cvt_pk_bf16_f32 v8, v8, v9
	v_cvt_pk_bf16_f32 v9, v10, v11
	v_cvt_pk_bf16_f32 v10, v16, v17
	v_cvt_pk_bf16_f32 v11, v14, v15
	v_add_co_u32_e32 v14, vcc, s66, v2
	v_pk_fma_f32 v[16:17], v[94:95], s[20:21], 0 op_sel_hi:[1,0,0]
	s_nop 0
	v_addc_co_u32_e32 v15, vcc, 0, v3, vcc
	ds_write_b128 v240, v[8:11]
	s_waitcnt lgkmcnt(1)
	global_store_dwordx4 v[244:245], v[246:249], off offset:256
	s_waitcnt lgkmcnt(0)
	s_barrier
	ds_read_b128 v[246:249], v241
	v_lshl_add_u64 v[244:245], v[14:15], 0, v[242:243]
	v_pk_fma_f32 v[14:15], v[96:97], s[20:21], 0 op_sel_hi:[1,0,0]
	s_nop 0
	v_pk_fma_f32 v[10:11], v[104:105], s[20:21], 0 op_sel_hi:[1,0,0]
	v_pk_fma_f32 v[8:9], v[102:103], s[20:21], 0 op_sel_hi:[1,0,0]
	s_nop 0
	v_cvt_pk_bf16_f32 v8, v8, v9
	v_cvt_pk_bf16_f32 v9, v10, v11
	v_cvt_pk_bf16_f32 v10, v16, v17
	v_cvt_pk_bf16_f32 v11, v14, v15
	ds_write_b128 v240, v[8:11] offset:8192
	s_waitcnt lgkmcnt(1)
	global_store_dwordx4 v[244:245], v[246:249], off
	s_waitcnt lgkmcnt(0)
	s_barrier
	ds_read_b128 v[246:249], v241 offset:8192
	v_lshl_add_u64 v[244:245], v[12:13], 0, v[242:243]
	v_pk_fma_f32 v[14:15], v[92:93], s[20:21], 0 op_sel_hi:[1,0,0]
	v_pk_fma_f32 v[16:17], v[90:91], s[20:21], 0 op_sel_hi:[1,0,0]
	v_pk_fma_f32 v[10:11], v[100:101], s[20:21], 0 op_sel_hi:[1,0,0]
	v_pk_fma_f32 v[8:9], v[98:99], s[20:21], 0 op_sel_hi:[1,0,0]
	v_lshl_add_u64 v[12:13], v[2:3], 0, s[38:39]
	v_cvt_pk_bf16_f32 v8, v8, v9
	v_cvt_pk_bf16_f32 v9, v10, v11
	v_cvt_pk_bf16_f32 v10, v16, v17
	v_cvt_pk_bf16_f32 v11, v14, v15
	v_add_co_u32_e32 v14, vcc, s67, v2
	v_pk_fma_f32 v[16:17], v[78:79], s[20:21], 0 op_sel_hi:[1,0,0]
	s_nop 0
	v_addc_co_u32_e32 v15, vcc, 0, v3, vcc
	ds_write_b128 v240, v[8:11]
	s_waitcnt lgkmcnt(1)
	global_store_dwordx4 v[244:245], v[246:249], off offset:256
	s_waitcnt lgkmcnt(0)
	s_barrier
	ds_read_b128 v[246:249], v241
	v_lshl_add_u64 v[244:245], v[14:15], 0, v[242:243]
	v_pk_fma_f32 v[14:15], v[80:81], s[20:21], 0 op_sel_hi:[1,0,0]
	s_nop 0
	v_pk_fma_f32 v[10:11], v[88:89], s[20:21], 0 op_sel_hi:[1,0,0]
	v_pk_fma_f32 v[8:9], v[86:87], s[20:21], 0 op_sel_hi:[1,0,0]
	s_nop 0
	v_cvt_pk_bf16_f32 v8, v8, v9
	v_cvt_pk_bf16_f32 v9, v10, v11
	v_cvt_pk_bf16_f32 v10, v16, v17
	v_cvt_pk_bf16_f32 v11, v14, v15
	ds_write_b128 v240, v[8:11] offset:8192
	s_waitcnt lgkmcnt(1)
	global_store_dwordx4 v[244:245], v[246:249], off
	s_waitcnt lgkmcnt(0)
	s_barrier
	ds_read_b128 v[246:249], v241 offset:8192
	v_lshl_add_u64 v[244:245], v[12:13], 0, v[242:243]
	v_lshl_add_u64 v[12:13], v[2:3], 0, s[40:41]
	v_add_co_u32_e32 v2, vcc, s68, v2
	v_pk_fma_f32 v[10:11], v[84:85], s[20:21], 0 op_sel_hi:[1,0,0]
	v_pk_fma_f32 v[8:9], v[82:83], s[20:21], 0 op_sel_hi:[1,0,0]
	v_pk_fma_f32 v[14:15], v[76:77], s[20:21], 0 op_sel_hi:[1,0,0]
	v_pk_fma_f32 v[16:17], v[74:75], s[20:21], 0 op_sel_hi:[1,0,0]
	v_cvt_pk_bf16_f32 v8, v8, v9
	v_cvt_pk_bf16_f32 v9, v10, v11
	v_addc_co_u32_e32 v3, vcc, 0, v3, vcc
	v_cvt_pk_bf16_f32 v10, v16, v17
	v_cvt_pk_bf16_f32 v11, v14, v15
	ds_write_b128 v240, v[8:11]
	s_waitcnt lgkmcnt(1)
	global_store_dwordx4 v[244:245], v[246:249], off offset:256
	s_waitcnt lgkmcnt(0)
	s_barrier
	ds_read_b128 v[246:249], v241
	v_lshl_add_u64 v[244:245], v[2:3], 0, v[242:243]
	s_andn2_b64 vcc, exec, s[42:43]
	s_mov_b64 s[42:43], -1
	v_pk_fma_f32 v[8:9], v[70:71], s[20:21], 0 op_sel_hi:[1,0,0]
	v_pk_fma_f32 v[10:11], v[66:67], s[20:21], 0 op_sel_hi:[1,0,0]
	v_pk_fma_f32 v[2:3], v[72:73], s[20:21], 0 op_sel_hi:[1,0,0]
	v_pk_fma_f32 v[14:15], v[68:69], s[20:21], 0 op_sel_hi:[1,0,0]
	v_cvt_pk_bf16_f32 v8, v8, v9
	v_cvt_pk_bf16_f32 v9, v2, v3
	v_cvt_pk_bf16_f32 v10, v10, v11
	s_nop 0
	v_cvt_pk_bf16_f32 v11, v14, v15
	ds_write_b128 v240, v[8:11] offset:8192
	s_waitcnt lgkmcnt(1)
	global_store_dwordx4 v[244:245], v[246:249], off
	s_waitcnt lgkmcnt(0)
	s_barrier
	ds_read_b128 v[246:249], v241 offset:8192
	v_lshl_add_u64 v[244:245], v[12:13], 0, v[242:243]
	s_waitcnt lgkmcnt(0)
	s_barrier
	global_store_dwordx4 v[244:245], v[246:249], off offset:256
	s_cbranch_vccnz .LBB0_1502
	s_andn2_b64 vcc, exec, s[14:15]
	s_cbranch_vccnz .LBB0_1501
	s_barrier
	s_branch .LBB0_1501

.LBB0_1891:
	v_lshl_or_b32 v18, s49, 8, v196
	s_ashr_i32 s49, s48, 31
	s_lshl_b64 s[48:49], s[48:49], 12
	s_add_u32 s48, s72, s48
	s_addc_u32 s49, s73, s49
	v_ashrrev_i32_e32 v19, 31, v18
	v_lshl_add_u64 v[2:3], v[18:19], 2, s[48:49]
	global_load_dwordx4 v[14:17], v[2:3], off
	global_load_dwordx4 v[10:13], v[2:3], off offset:16
	global_load_dwordx4 v[6:9], v[2:3], off offset:512
	s_nop 0
	global_load_dwordx4 v[2:5], v[2:3], off offset:528
	v_lshl_add_u32 v24, s84, 8, v195
	v_ashrrev_i32_e32 v25, 31, v24
	v_or_b32_e32 v26, 16, v24
	v_or_b32_e32 v28, 32, v24
	v_or_b32_e32 v30, 48, v24
	v_lshlrev_b64 v[24:25], 11, v[24:25]
	v_ashrrev_i32_e32 v27, 31, v26
	v_ashrrev_i32_e32 v29, 31, v28
	v_lshlrev_b64 v[32:33], 1, v[18:19]
	v_ashrrev_i32_e32 v31, 31, v30
	v_lshl_add_u64 v[18:19], s[28:29], 0, v[24:25]
	v_lshlrev_b64 v[24:25], 11, v[26:27]
	v_lshlrev_b64 v[26:27], 11, v[28:29]
	v_lshlrev_b64 v[28:29], 11, v[30:31]
	v_lshl_add_u64 v[24:25], s[28:29], 0, v[24:25]
	v_lshl_add_u64 v[26:27], s[28:29], 0, v[26:27]
	v_lshl_add_u64 v[28:29], s[28:29], 0, v[28:29]
	v_lshl_add_u64 v[30:31], v[24:25], 0, v[32:33]
	v_lshl_add_u64 v[34:35], v[26:27], 0, v[32:33]
	v_lshl_add_u64 v[18:19], v[18:19], 0, v[32:33]
	v_lshl_add_u64 v[28:29], v[28:29], 0, v[32:33]
	s_waitcnt vmcnt(3)
	v_pk_fma_f32 v[26:27], v[192:193], s[30:31], v[16:17] op_sel_hi:[1,0,1]
	v_pk_fma_f32 v[24:25], v[190:191], s[30:31], v[14:15] op_sel_hi:[1,0,1]
	s_waitcnt vmcnt(2)
	v_pk_fma_f32 v[32:33], v[188:189], s[30:31], v[12:13] op_sel_hi:[1,0,1]
	v_pk_fma_f32 v[36:37], v[186:187], s[30:31], v[10:11] op_sel_hi:[1,0,1]
	v_cvt_pk_bf16_f32 v24, v24, v25
	v_cvt_pk_bf16_f32 v25, v26, v27
	s_waitcnt vmcnt(1)
	v_pk_fma_f32 v[38:39], v[172:173], s[30:31], v[8:9] op_sel_hi:[1,0,1]
	v_cvt_pk_bf16_f32 v26, v36, v37
	v_cvt_pk_bf16_f32 v27, v32, v33
	v_pk_fma_f32 v[40:41], v[170:171], s[30:31], v[6:7] op_sel_hi:[1,0,1]
	s_waitcnt vmcnt(0)
	v_pk_fma_f32 v[42:43], v[164:165], s[30:31], v[4:5] op_sel_hi:[1,0,1]
	v_pk_fma_f32 v[44:45], v[162:163], s[30:31], v[2:3] op_sel_hi:[1,0,1]
	ds_write_b128 v240, v[24:27]
	s_waitcnt lgkmcnt(0)
	s_barrier
	ds_read_b128 v[246:249], v241
	v_lshl_add_u64 v[244:245], v[18:19], 0, v[242:243]
	v_pk_fma_f32 v[46:47], v[184:185], s[30:31], v[16:17] op_sel_hi:[1,0,1]
	v_pk_fma_f32 v[48:49], v[182:183], s[30:31], v[14:15] op_sel_hi:[1,0,1]
	v_cvt_pk_bf16_f32 v24, v40, v41
	v_cvt_pk_bf16_f32 v25, v38, v39
	v_cvt_pk_bf16_f32 v26, v44, v45
	v_cvt_pk_bf16_f32 v27, v42, v43
	v_pk_fma_f32 v[50:51], v[180:181], s[30:31], v[12:13] op_sel_hi:[1,0,1]
	v_pk_fma_f32 v[52:53], v[178:179], s[30:31], v[10:11] op_sel_hi:[1,0,1]
	ds_write_b128 v240, v[24:27] offset:8192
	s_waitcnt lgkmcnt(1)
	global_store_dwordx4 v[244:245], v[246:249], off
	s_waitcnt lgkmcnt(0)
	s_barrier
	ds_read_b128 v[246:249], v241 offset:8192
	v_lshl_add_u64 v[244:245], v[18:19], 0, v[242:243]
	v_pk_fma_f32 v[54:55], v[156:157], s[30:31], v[8:9] op_sel_hi:[1,0,1]
	v_pk_fma_f32 v[56:57], v[154:155], s[30:31], v[6:7] op_sel_hi:[1,0,1]
	v_cvt_pk_bf16_f32 v24, v48, v49
	v_cvt_pk_bf16_f32 v25, v46, v47
	v_cvt_pk_bf16_f32 v26, v52, v53
	v_cvt_pk_bf16_f32 v27, v50, v51
	v_pk_fma_f32 v[58:59], v[148:149], s[30:31], v[4:5] op_sel_hi:[1,0,1]
	v_pk_fma_f32 v[60:61], v[146:147], s[30:31], v[2:3] op_sel_hi:[1,0,1]
	ds_write_b128 v240, v[24:27]
	s_waitcnt lgkmcnt(1)
	global_store_dwordx4 v[244:245], v[246:249], off offset:256
	s_waitcnt lgkmcnt(0)
	s_barrier
	ds_read_b128 v[246:249], v241
	v_lshl_add_u64 v[244:245], v[30:31], 0, v[242:243]
	v_pk_fma_f32 v[62:63], v[176:177], s[30:31], v[16:17] op_sel_hi:[1,0,1]
	v_pk_fma_f32 v[64:65], v[174:175], s[30:31], v[14:15] op_sel_hi:[1,0,1]
	v_cvt_pk_bf16_f32 v24, v56, v57
	v_cvt_pk_bf16_f32 v25, v54, v55
	v_cvt_pk_bf16_f32 v26, v60, v61
	v_cvt_pk_bf16_f32 v27, v58, v59
	v_pk_fma_f32 v[146:147], v[168:169], s[30:31], v[12:13] op_sel_hi:[1,0,1]
	v_pk_fma_f32 v[148:149], v[166:167], s[30:31], v[10:11] op_sel_hi:[1,0,1]
	ds_write_b128 v240, v[24:27] offset:8192
	s_waitcnt lgkmcnt(1)
	global_store_dwordx4 v[244:245], v[246:249], off
	s_waitcnt lgkmcnt(0)
	s_barrier
	ds_read_b128 v[246:249], v241 offset:8192
	v_lshl_add_u64 v[244:245], v[30:31], 0, v[242:243]
	v_pk_fma_f32 v[144:145], v[144:145], s[30:31], v[8:9] op_sel_hi:[1,0,1]
	v_pk_fma_f32 v[142:143], v[142:143], s[30:31], v[6:7] op_sel_hi:[1,0,1]
	v_cvt_pk_bf16_f32 v24, v64, v65
	v_cvt_pk_bf16_f32 v25, v62, v63
	v_cvt_pk_bf16_f32 v26, v148, v149
	v_cvt_pk_bf16_f32 v27, v146, v147
	v_pk_fma_f32 v[140:141], v[140:141], s[30:31], v[4:5] op_sel_hi:[1,0,1]
	v_pk_fma_f32 v[138:139], v[138:139], s[30:31], v[2:3] op_sel_hi:[1,0,1]
	ds_write_b128 v240, v[24:27]
	s_waitcnt lgkmcnt(1)
	global_store_dwordx4 v[244:245], v[246:249], off offset:256
	s_waitcnt lgkmcnt(0)
	s_barrier
	ds_read_b128 v[246:249], v241
	v_lshl_add_u64 v[244:245], v[34:35], 0, v[242:243]
	v_pk_fma_f32 v[154:155], v[160:161], s[30:31], v[16:17] op_sel_hi:[1,0,1]
	v_pk_fma_f32 v[156:157], v[158:159], s[30:31], v[14:15] op_sel_hi:[1,0,1]
	v_cvt_pk_bf16_f32 v24, v142, v143
	v_cvt_pk_bf16_f32 v25, v144, v145
	v_cvt_pk_bf16_f32 v26, v138, v139
	v_cvt_pk_bf16_f32 v27, v140, v141
	v_pk_fma_f32 v[152:153], v[152:153], s[30:31], v[12:13] op_sel_hi:[1,0,1]
	v_pk_fma_f32 v[150:151], v[150:151], s[30:31], v[10:11] op_sel_hi:[1,0,1]
	ds_write_b128 v240, v[24:27] offset:8192
	s_waitcnt lgkmcnt(1)
	global_store_dwordx4 v[244:245], v[246:249], off
	s_waitcnt lgkmcnt(0)
	s_barrier
	ds_read_b128 v[246:249], v241 offset:8192
	v_lshl_add_u64 v[244:245], v[34:35], 0, v[242:243]
	v_pk_fma_f32 v[30:31], v[132:133], s[30:31], v[4:5] op_sel_hi:[1,0,1]
	v_pk_fma_f32 v[32:33], v[130:131], s[30:31], v[2:3] op_sel_hi:[1,0,1]
	v_cvt_pk_bf16_f32 v24, v156, v157
	v_cvt_pk_bf16_f32 v25, v154, v155
	v_cvt_pk_bf16_f32 v26, v150, v151
	v_cvt_pk_bf16_f32 v27, v152, v153
	ds_write_b128 v240, v[24:27]
	s_waitcnt lgkmcnt(1)
	global_store_dwordx4 v[244:245], v[246:249], off offset:256
	s_waitcnt lgkmcnt(0)
	s_barrier
	ds_read_b128 v[246:249], v241
	v_lshl_add_u64 v[244:245], v[28:29], 0, v[242:243]
	s_nop 1
	v_pk_fma_f32 v[26:27], v[136:137], s[30:31], v[8:9] op_sel_hi:[1,0,1]
	v_pk_fma_f32 v[24:25], v[134:135], s[30:31], v[6:7] op_sel_hi:[1,0,1]
	s_nop 0
	v_cvt_pk_bf16_f32 v24, v24, v25
	v_cvt_pk_bf16_f32 v25, v26, v27
	v_cvt_pk_bf16_f32 v26, v32, v33
	v_cvt_pk_bf16_f32 v27, v30, v31
	ds_write_b128 v240, v[24:27] offset:8192
	s_waitcnt lgkmcnt(1)
	global_store_dwordx4 v[244:245], v[246:249], off
	s_waitcnt lgkmcnt(0)
	s_barrier
	ds_read_b128 v[246:249], v241 offset:8192
	v_lshl_add_u64 v[244:245], v[28:29], 0, v[242:243]
	v_pk_fma_f32 v[30:31], v[124:125], s[30:31], v[12:13] op_sel_hi:[1,0,1]
	v_pk_fma_f32 v[32:33], v[122:123], s[30:31], v[10:11] op_sel_hi:[1,0,1]
	v_pk_fma_f32 v[26:27], v[128:129], s[30:31], v[16:17] op_sel_hi:[1,0,1]
	v_pk_fma_f32 v[24:25], v[126:127], s[30:31], v[14:15] op_sel_hi:[1,0,1]
	v_lshl_add_u64 v[28:29], v[18:19], 0, s[38:39]
	v_cvt_pk_bf16_f32 v24, v24, v25
	v_cvt_pk_bf16_f32 v25, v26, v27
	v_cvt_pk_bf16_f32 v26, v32, v33
	v_cvt_pk_bf16_f32 v27, v30, v31
	v_add_co_u32_e32 v30, vcc, s80, v18
	v_pk_fma_f32 v[32:33], v[110:111], s[30:31], v[2:3] op_sel_hi:[1,0,1]
	s_nop 0
	v_addc_co_u32_e32 v31, vcc, 0, v19, vcc
	ds_write_b128 v240, v[24:27]
	s_waitcnt lgkmcnt(1)
	global_store_dwordx4 v[244:245], v[246:249], off offset:256
	s_waitcnt lgkmcnt(0)
	s_barrier
	ds_read_b128 v[246:249], v241
	v_lshl_add_u64 v[244:245], v[30:31], 0, v[242:243]
	v_pk_fma_f32 v[30:31], v[112:113], s[30:31], v[4:5] op_sel_hi:[1,0,1]
	s_nop 0
	v_pk_fma_f32 v[26:27], v[120:121], s[30:31], v[8:9] op_sel_hi:[1,0,1]
	v_pk_fma_f32 v[24:25], v[118:119], s[30:31], v[6:7] op_sel_hi:[1,0,1]
	s_nop 0
	v_cvt_pk_bf16_f32 v24, v24, v25
	v_cvt_pk_bf16_f32 v25, v26, v27
	v_cvt_pk_bf16_f32 v26, v32, v33
	v_cvt_pk_bf16_f32 v27, v30, v31
	ds_write_b128 v240, v[24:27] offset:8192
	s_waitcnt lgkmcnt(1)
	global_store_dwordx4 v[244:245], v[246:249], off
	s_waitcnt lgkmcnt(0)
	s_barrier
	ds_read_b128 v[246:249], v241 offset:8192
	v_lshl_add_u64 v[244:245], v[28:29], 0, v[242:243]
	v_pk_fma_f32 v[30:31], v[108:109], s[30:31], v[12:13] op_sel_hi:[1,0,1]
	v_pk_fma_f32 v[32:33], v[106:107], s[30:31], v[10:11] op_sel_hi:[1,0,1]
	v_pk_fma_f32 v[26:27], v[116:117], s[30:31], v[16:17] op_sel_hi:[1,0,1]
	v_pk_fma_f32 v[24:25], v[114:115], s[30:31], v[14:15] op_sel_hi:[1,0,1]
	v_lshl_add_u64 v[28:29], v[18:19], 0, s[40:41]
	v_cvt_pk_bf16_f32 v24, v24, v25
	v_cvt_pk_bf16_f32 v25, v26, v27
	v_cvt_pk_bf16_f32 v26, v32, v33
	v_cvt_pk_bf16_f32 v27, v30, v31
	v_add_co_u32_e32 v30, vcc, s81, v18
	v_pk_fma_f32 v[32:33], v[94:95], s[30:31], v[2:3] op_sel_hi:[1,0,1]
	s_nop 0
	v_addc_co_u32_e32 v31, vcc, 0, v19, vcc
	ds_write_b128 v240, v[24:27]
	s_waitcnt lgkmcnt(1)
	global_store_dwordx4 v[244:245], v[246:249], off offset:256
	s_waitcnt lgkmcnt(0)
	s_barrier
	ds_read_b128 v[246:249], v241
	v_lshl_add_u64 v[244:245], v[30:31], 0, v[242:243]
	v_pk_fma_f32 v[30:31], v[96:97], s[30:31], v[4:5] op_sel_hi:[1,0,1]
	s_nop 0
	v_pk_fma_f32 v[26:27], v[104:105], s[30:31], v[8:9] op_sel_hi:[1,0,1]
	v_pk_fma_f32 v[24:25], v[102:103], s[30:31], v[6:7] op_sel_hi:[1,0,1]
	s_nop 0
	v_cvt_pk_bf16_f32 v24, v24, v25
	v_cvt_pk_bf16_f32 v25, v26, v27
	v_cvt_pk_bf16_f32 v26, v32, v33
	v_cvt_pk_bf16_f32 v27, v30, v31
	ds_write_b128 v240, v[24:27] offset:8192
	s_waitcnt lgkmcnt(1)
	global_store_dwordx4 v[244:245], v[246:249], off
	s_waitcnt lgkmcnt(0)
	s_barrier
	ds_read_b128 v[246:249], v241 offset:8192
	v_lshl_add_u64 v[244:245], v[28:29], 0, v[242:243]
	v_pk_fma_f32 v[30:31], v[92:93], s[30:31], v[12:13] op_sel_hi:[1,0,1]
	v_pk_fma_f32 v[32:33], v[90:91], s[30:31], v[10:11] op_sel_hi:[1,0,1]
	v_pk_fma_f32 v[26:27], v[100:101], s[30:31], v[16:17] op_sel_hi:[1,0,1]
	v_pk_fma_f32 v[24:25], v[98:99], s[30:31], v[14:15] op_sel_hi:[1,0,1]
	v_lshl_add_u64 v[28:29], v[18:19], 0, s[42:43]
	v_cvt_pk_bf16_f32 v24, v24, v25
	v_cvt_pk_bf16_f32 v25, v26, v27
	v_cvt_pk_bf16_f32 v26, v32, v33
	v_cvt_pk_bf16_f32 v27, v30, v31
	v_add_co_u32_e32 v30, vcc, s82, v18
	v_pk_fma_f32 v[32:33], v[78:79], s[30:31], v[2:3] op_sel_hi:[1,0,1]
	s_nop 0
	v_addc_co_u32_e32 v31, vcc, 0, v19, vcc
	ds_write_b128 v240, v[24:27]
	s_waitcnt lgkmcnt(1)
	global_store_dwordx4 v[244:245], v[246:249], off offset:256
	s_waitcnt lgkmcnt(0)
	s_barrier
	ds_read_b128 v[246:249], v241
	v_lshl_add_u64 v[244:245], v[30:31], 0, v[242:243]
	v_pk_fma_f32 v[30:31], v[80:81], s[30:31], v[4:5] op_sel_hi:[1,0,1]
	v_pk_fma_f32 v[14:15], v[82:83], s[30:31], v[14:15] op_sel_hi:[1,0,1]
	v_pk_fma_f32 v[26:27], v[88:89], s[30:31], v[8:9] op_sel_hi:[1,0,1]
	v_pk_fma_f32 v[24:25], v[86:87], s[30:31], v[6:7] op_sel_hi:[1,0,1]
	v_pk_fma_f32 v[16:17], v[84:85], s[30:31], v[16:17] op_sel_hi:[1,0,1]
	v_cvt_pk_bf16_f32 v24, v24, v25
	v_cvt_pk_bf16_f32 v25, v26, v27
	v_cvt_pk_bf16_f32 v26, v32, v33
	v_cvt_pk_bf16_f32 v27, v30, v31
	ds_write_b128 v240, v[24:27] offset:8192
	s_waitcnt lgkmcnt(1)
	global_store_dwordx4 v[244:245], v[246:249], off
	s_waitcnt lgkmcnt(0)
	s_barrier
	ds_read_b128 v[246:249], v241 offset:8192
	v_lshl_add_u64 v[244:245], v[28:29], 0, v[242:243]
	v_pk_fma_f32 v[8:9], v[72:73], s[30:31], v[8:9] op_sel_hi:[1,0,1]
	v_pk_fma_f32 v[6:7], v[70:71], s[30:31], v[6:7] op_sel_hi:[1,0,1]
	v_pk_fma_f32 v[26:27], v[76:77], s[30:31], v[12:13] op_sel_hi:[1,0,1]
	v_pk_fma_f32 v[12:13], v[74:75], s[30:31], v[10:11] op_sel_hi:[1,0,1]
	v_cvt_pk_bf16_f32 v10, v14, v15
	v_add_co_u32_e32 v14, vcc, s83, v18
	v_cvt_pk_bf16_f32 v11, v16, v17
	v_lshl_add_u64 v[24:25], v[18:19], 0, s[44:45]
	s_nop 0
	v_addc_co_u32_e32 v15, vcc, 0, v19, vcc
	v_cvt_pk_bf16_f32 v12, v12, v13
	v_cvt_pk_bf16_f32 v13, v26, v27
	ds_write_b128 v240, v[10:13]
	s_waitcnt lgkmcnt(1)
	global_store_dwordx4 v[244:245], v[246:249], off offset:256
	s_waitcnt lgkmcnt(0)
	s_barrier
	ds_read_b128 v[246:249], v241
	v_lshl_add_u64 v[244:245], v[14:15], 0, v[242:243]
	s_andn2_b64 vcc, exec, s[46:47]
	s_mov_b64 s[46:47], -1
	v_pk_fma_f32 v[10:11], v[68:69], s[30:31], v[4:5] op_sel_hi:[1,0,1]
	v_pk_fma_f32 v[4:5], v[66:67], s[30:31], v[2:3] op_sel_hi:[1,0,1]
	v_cvt_pk_bf16_f32 v2, v6, v7
	v_cvt_pk_bf16_f32 v3, v8, v9
	s_nop 0
	v_cvt_pk_bf16_f32 v4, v4, v5
	v_cvt_pk_bf16_f32 v5, v10, v11
	ds_write_b128 v240, v[2:5] offset:8192
	s_waitcnt lgkmcnt(1)
	global_store_dwordx4 v[244:245], v[246:249], off
	s_waitcnt lgkmcnt(0)
	s_barrier
	ds_read_b128 v[246:249], v241 offset:8192
	v_lshl_add_u64 v[244:245], v[24:25], 0, v[242:243]
	s_waitcnt lgkmcnt(0)
	s_barrier
	global_store_dwordx4 v[244:245], v[246:249], off offset:256
	s_cbranch_vccnz .LBB0_1865
	s_andn2_b64 vcc, exec, s[20:21]
	s_cbranch_vccnz .LBB0_1864
	s_barrier
	s_branch .LBB0_1864
